# bundle: attention LDS swizzle, MoE scheduler ballot, accumulator zeroing via MFMA, N2 router biases from LDS
# speedup vs baseline: 1.0107x; 1.0034x over previous
.LBB0_260:
	s_mov_b32 s20, s37
	s_mov_b32 s38, s37
	s_add_i32 s37, s37, 1
	s_cmp_lt_u32 s38, 11
	s_cselect_b64 s[8:9], -1, 0
	s_and_b64 s[18:19], s[8:9], exec
	s_cselect_b32 s18, s37, s20
	s_ashr_i32 s19, s18, 31
	s_lshl_b64 s[18:19], s[18:19], 18
	s_add_u32 s18, s10, s18
	s_addc_u32 s19, s11, s19
	s_and_b64 s[8:9], s[8:9], exec
	s_cselect_b32 s22, s19, s7
	s_cselect_b32 s23, s18, s6
	s_add_u32 s39, s6, 0x100
	s_addc_u32 s49, s7, 0
	v_mov_b32_e32 v0, 0
	v_readlane_b32 s6, v254, 51
	s_mov_b32 s56, -2
	v_readlane_b32 s7, v254, 52
	v_mov_b32_e32 v1, v0
	v_mov_b32_e32 v2, v0
	v_mov_b32_e32 v3, v0
	v_mov_b32_e32 v4, v0
	v_mov_b32_e32 v5, v0
	v_mov_b32_e32 v6, v0
	v_mov_b32_e32 v7, v0
	v_mov_b32_e32 v8, v0
	v_mov_b32_e32 v9, v0
	v_mov_b32_e32 v10, v0
	v_mov_b32_e32 v11, v0
	v_mov_b32_e32 v12, v0
	v_mov_b32_e32 v13, v0
	v_mov_b32_e32 v14, v0
	v_mov_b32_e32 v15, v0
	v_mfma_f32_32x32x16_bf16 v[16:31], v[0:3], v[0:3], 0
	v_mfma_f32_32x32x16_bf16 v[32:47], v[0:3], v[0:3], 0
	v_mfma_f32_32x32x16_bf16 v[48:63], v[0:3], v[0:3], 0
	v_mfma_f32_32x32x16_bf16 v[66:81], v[0:3], v[0:3], 0
	v_mfma_f32_32x32x16_bf16 v[82:97], v[0:3], v[0:3], 0
	v_mfma_f32_32x32x16_bf16 v[98:113], v[0:3], v[0:3], 0
	v_mfma_f32_32x32x16_bf16 v[114:129], v[0:3], v[0:3], 0

.LBB0_354:
	s_mov_b32 s18, s30
	s_mov_b32 s31, s30
	s_add_i32 s30, s30, 1
	s_cmp_lt_u32 s31, 10
	s_cselect_b64 s[16:17], -1, 0
	s_and_b64 s[12:13], s[16:17], exec
	s_cselect_b32 s12, s30, s18
	s_ashr_i32 s13, s12, 31
	s_lshl_b64 s[12:13], s[12:13], 19
	s_add_u32 s12, s6, s12
	s_addc_u32 s13, s7, s13
	s_and_b64 s[16:17], s[16:17], exec
	s_cselect_b32 s34, s13, s15
	s_cselect_b32 s35, s12, s14
	s_add_u32 s36, s14, 0x100
	s_addc_u32 s37, s15, 0
	v_mov_b32_e32 v0, 0
	v_readlane_b32 s14, v254, 53
	s_mov_b32 s38, -2
	v_readlane_b32 s15, v254, 54
	v_mov_b32_e32 v1, v0
	v_mov_b32_e32 v2, v0
	v_mov_b32_e32 v3, v0
	v_mov_b32_e32 v4, v0
	v_mov_b32_e32 v5, v0
	v_mov_b32_e32 v6, v0
	v_mov_b32_e32 v7, v0
	v_mov_b32_e32 v8, v0
	v_mov_b32_e32 v9, v0
	v_mov_b32_e32 v10, v0
	v_mov_b32_e32 v11, v0
	v_mov_b32_e32 v12, v0
	v_mov_b32_e32 v13, v0
	v_mov_b32_e32 v14, v0
	v_mov_b32_e32 v15, v0
	v_mfma_f32_32x32x16_bf16 v[16:31], v[0:3], v[0:3], 0
	v_mfma_f32_32x32x16_bf16 v[32:47], v[0:3], v[0:3], 0
	v_mfma_f32_32x32x16_bf16 v[48:63], v[0:3], v[0:3], 0
	v_mfma_f32_32x32x16_bf16 v[66:81], v[0:3], v[0:3], 0
	v_mfma_f32_32x32x16_bf16 v[82:97], v[0:3], v[0:3], 0
	v_mfma_f32_32x32x16_bf16 v[98:113], v[0:3], v[0:3], 0
	v_mfma_f32_32x32x16_bf16 v[114:129], v[0:3], v[0:3], 0

.LBB0_671:
	s_mov_b32 s18, s31
	s_mov_b32 s34, s31
	s_add_i32 s31, s31, 1
	s_cmp_lt_u32 s34, 3
	s_cselect_b64 s[16:17], -1, 0
	s_and_b64 s[12:13], s[16:17], exec
	s_cselect_b32 s12, s31, s18
	s_ashr_i32 s13, s12, 31
	s_lshl_b64 s[12:13], s[12:13], 18
	s_add_u32 s12, s6, s12
	s_addc_u32 s13, s7, s13
	s_and_b64 s[16:17], s[16:17], exec
	s_cselect_b32 s35, s13, s15
	s_cselect_b32 s36, s12, s14
	s_add_u32 s37, s14, 0x100
	s_addc_u32 s38, s15, 0
	v_mov_b32_e32 v0, 0
	v_readlane_b32 s14, v254, 56
	s_mov_b32 s39, -2
	v_readlane_b32 s15, v254, 57
	v_mov_b32_e32 v1, v0
	v_mov_b32_e32 v2, v0
	v_mov_b32_e32 v3, v0
	v_mov_b32_e32 v4, v0
	v_mov_b32_e32 v5, v0
	v_mov_b32_e32 v6, v0
	v_mov_b32_e32 v7, v0
	v_mov_b32_e32 v12, v0
	v_mov_b32_e32 v13, v0
	v_mov_b32_e32 v14, v0
	v_mov_b32_e32 v15, v0
	v_mov_b32_e32 v8, v0
	v_mov_b32_e32 v9, v0
	v_mov_b32_e32 v10, v0
	v_mov_b32_e32 v11, v0
	v_mfma_f32_32x32x16_bf16 v[16:31], v[0:3], v[0:3], 0
	v_mfma_f32_32x32x16_bf16 v[32:47], v[0:3], v[0:3], 0
	v_mfma_f32_32x32x16_bf16 v[48:63], v[0:3], v[0:3], 0
	v_mfma_f32_32x32x16_bf16 v[66:81], v[0:3], v[0:3], 0
	v_mfma_f32_32x32x16_bf16 v[82:97], v[0:3], v[0:3], 0
	v_mfma_f32_32x32x16_bf16 v[98:113], v[0:3], v[0:3], 0
	v_mfma_f32_32x32x16_bf16 v[114:129], v[0:3], v[0:3], 0

.LBB0_685:
	s_mov_b32 s18, s29
	s_mov_b32 s30, s29
	s_add_i32 s29, s29, 1
	s_cmp_lt_u32 s30, 3
	s_cselect_b64 s[16:17], -1, 0
	s_and_b64 s[12:13], s[16:17], exec
	s_cselect_b32 s12, s29, s18
	s_ashr_i32 s13, s12, 31
	s_lshl_b64 s[12:13], s[12:13], 19
	s_add_u32 s12, s6, s12
	s_addc_u32 s13, s7, s13
	s_and_b64 s[16:17], s[16:17], exec
	s_cselect_b32 s31, s13, s15
	s_cselect_b32 s34, s12, s14
	s_add_u32 s35, s14, 0x100
	s_addc_u32 s36, s15, 0
	v_mov_b32_e32 v0, 0
	v_readlane_b32 s14, v254, 58
	s_mov_b32 s37, -2
	v_readlane_b32 s15, v254, 59
	v_mov_b32_e32 v1, v0
	v_mov_b32_e32 v2, v0
	v_mov_b32_e32 v3, v0
	v_mov_b32_e32 v4, v0
	v_mov_b32_e32 v5, v0
	v_mov_b32_e32 v6, v0
	v_mov_b32_e32 v7, v0
	v_mov_b32_e32 v8, v0
	v_mov_b32_e32 v9, v0
	v_mov_b32_e32 v10, v0
	v_mov_b32_e32 v11, v0
	v_mov_b32_e32 v12, v0
	v_mov_b32_e32 v13, v0
	v_mov_b32_e32 v14, v0
	v_mov_b32_e32 v15, v0
	v_mfma_f32_32x32x16_bf16 v[16:31], v[0:3], v[0:3], 0
	v_mfma_f32_32x32x16_bf16 v[32:47], v[0:3], v[0:3], 0
	v_mfma_f32_32x32x16_bf16 v[48:63], v[0:3], v[0:3], 0
	v_mfma_f32_32x32x16_bf16 v[66:81], v[0:3], v[0:3], 0
	v_mfma_f32_32x32x16_bf16 v[82:97], v[0:3], v[0:3], 0
	v_mfma_f32_32x32x16_bf16 v[98:113], v[0:3], v[0:3], 0
	v_mfma_f32_32x32x16_bf16 v[114:129], v[0:3], v[0:3], 0

.LBB0_693:
	v_readlane_b32 s22, v254, 12
	s_mov_b32 s6, s22
	s_waitcnt vmcnt(0)
	s_barrier
	v_mbcnt_lo_u32_b32 v0, -1, 0
	v_mbcnt_hi_u32_b32 v0, -1, v0
	v_mbcnt_lo_u32_b32 v222, -1, 0
	v_mbcnt_hi_u32_b32 v222, -1, v222
	s_nop 0
	v_lshl_add_u32 v130, s22, 6, v222
	v_cmp_gt_i32_e64 s[6:7], 32, v130
	v_lshl_add_u32 v230, v130, 2, 0
	s_barrier
	s_and_saveexec_b64 s[8:9], s[6:7]
	v_add_u32_e32 v0, 0x22c00, v230
	ds_write_b32 v0, v65
	s_or_b64 exec, exec, s[8:9]
	v_readlane_b32 s18, v255, 37
	v_readlane_b32 s19, v255, 38
	s_mov_b32 s19, s67
	s_lshl_b64 s[10:11], s[18:19], 3
	s_mul_i32 s9, s18, 0x30000
	v_readlane_b32 s12, v255, 26
	s_mul_hi_u32 s8, s18, 0x30000
	v_readlane_b32 s13, v255, 27
	s_add_u32 s16, s12, s9
	s_addc_u32 s17, s13, s8
	s_mov_b32 s8, s18
	s_add_u32 s14, s16, 0x18000
	v_writelane_b32 v255, s8, 37
	v_readlane_b32 s28, v254, 13
	s_addc_u32 s15, s17, 0
	v_writelane_b32 v255, s9, 38
	s_add_i32 s8, s22, s28
	s_ashr_i32 s9, s8, 8
	s_lshl_b32 s66, s18, 2
	s_ashr_i32 s12, s9, 31
	s_add_u32 s9, s10, s9
	s_addc_u32 s10, s11, s12
	s_mulk_i32 s10, 0x6000
	s_mul_hi_u32 s11, s9, 0x6000
	s_add_i32 s11, s11, s10
	s_mulk_i32 s9, 0x6000
	v_readlane_b32 s12, v255, 28
	v_readlane_b32 s13, v255, 29
	s_add_u32 s9, s12, s9
	s_addc_u32 s23, s13, s11
	v_readlane_b32 s26, v254, 16
	v_readlane_b32 s20, v255, 39
	v_readlane_b32 s27, v254, 17
	s_load_dwordx2 s[18:19], s[26:27], 48
	s_waitcnt lgkmcnt(0)
	v_readlane_b32 s21, v255, 40
	s_add_u32 s20, s18, s20
	s_addc_u32 s21, s19, s21
	v_and_b32_e32 v153, 63, v222
	s_load_dwordx2 s[12:13], s[26:27], 0x98
	s_waitcnt lgkmcnt(0)
	s_add_u32 s18, s9, 0x4000
	s_load_dwordx2 s[10:11], s[26:27], 0xa8
	s_waitcnt lgkmcnt(0)
	s_addc_u32 s19, s23, 0
	v_lshlrev_b32_e32 v152, 4, v153
	global_load_dwordx4 v[60:63], v152, s[18:19]
	v_or_b32_e32 v8, 0x400, v152
	global_load_dwordx4 v[66:69], v8, s[18:19]
	global_load_dwordx4 v[70:73], v152, s[20:21]
	global_load_dwordx4 v[74:77], v152, s[20:21] offset:1024
	global_load_dwordx4 v[142:145], v152, s[20:21] offset:2048
	global_load_dwordx4 v[146:149], v152, s[20:21] offset:3072
	s_add_u32 s20, s9, 0x3000
	s_addc_u32 s21, s23, 0
	s_add_u32 s24, s9, 0x2000
	s_addc_u32 s25, s23, 0
	v_or_b32_e32 v24, 0x800, v152
	v_or_b32_e32 v42, 0xc00, v152
	global_load_dwordx4 v[0:3], v8, s[24:25]
	global_load_dwordx4 v[154:157], v24, s[18:19]
	global_load_dwordx4 v[4:7], v152, s[20:21]
	s_nop 0
	global_load_dwordx4 v[8:11], v8, s[20:21]
	s_nop 0
	global_load_dwordx4 v[158:161], v42, s[18:19]
	global_load_dwordx4 v[12:15], v42, s[20:21]
	v_and_b32_e32 v162, 15, v222
	s_lshl_b32 s9, s22, 7
	v_bfe_u32 v163, v222, 4, 2
	v_lshlrev_b32_e32 v64, 10, v162
	s_ashr_i32 s18, s9, 31
	v_mov_b32_e32 v103, v65
	v_or_b32_e32 v102, 0x4000, v64
	v_lshl_or_b32 v120, v163, 3, s9
	v_mov_b32_e32 v121, s18
	v_mov_b32_e32 v119, v65
	v_or_b32_e32 v118, 0x8000, v64
	v_or_b32_e32 v28, 32, v120
	v_lshl_add_u64 v[32:33], v[120:121], 0, v[102:103]
	v_mov_b32_e32 v29, s18
	v_lshl_add_u64 v[30:31], v[120:121], 0, v[64:65]
	v_lshl_add_u64 v[34:35], v[120:121], 0, v[118:119]
	v_lshlrev_b64 v[32:33], 1, v[32:33]
	v_lshl_add_u64 v[36:37], v[28:29], 0, v[64:65]
	v_lshl_add_u64 v[38:39], v[28:29], 0, v[102:103]
	v_lshlrev_b64 v[30:31], 1, v[30:31]
	v_lshlrev_b64 v[34:35], 1, v[34:35]
	v_lshl_add_u64 v[28:29], v[28:29], 0, v[118:119]
	v_lshl_add_u64 v[40:41], s[14:15], 0, v[32:33]
	v_lshl_add_u64 v[52:53], v[36:37], 1, s[14:15]
	v_lshl_add_u64 v[56:57], v[38:39], 1, s[14:15]
	global_load_dwordx4 v[16:19], v152, s[24:25]
	global_load_dwordx4 v[20:23], v24, s[20:21]
	s_nop 0
	global_load_dwordx4 v[24:27], v24, s[24:25]
	v_lshl_add_u64 v[98:99], s[16:17], 0, v[30:31]
	v_lshl_add_u64 v[94:95], s[14:15], 0, v[30:31]
	v_lshl_add_u64 v[106:107], s[16:17], 0, v[32:33]
	v_lshl_add_u64 v[122:123], s[16:17], 0, v[34:35]
	v_lshl_add_u64 v[124:125], s[14:15], 0, v[34:35]
	v_lshl_add_u64 v[80:81], v[28:29], 1, s[14:15]
	global_load_dwordx4 v[28:31], v42, s[24:25]
	global_load_dwordx4 v[32:35], v[98:99], off
	global_load_dwordx4 v[36:39], v[40:41], off
	s_nop 0
	global_load_dwordx4 v[40:43], v[122:123], off
	global_load_dwordx4 v[44:47], v[106:107], off
	global_load_dwordx4 v[48:51], v[106:107], off offset:64
	s_nop 0
	global_load_dwordx4 v[52:55], v[52:53], off
	s_nop 0
	global_load_dwordx4 v[56:59], v[56:57], off
	v_or_b32_e32 v78, 64, v120
	v_mov_b32_e32 v79, s18
	v_or_b32_e32 v120, 0x60, v120
	v_lshl_add_u64 v[88:89], v[78:79], 0, v[118:119]
	v_lshl_add_u64 v[104:105], v[120:121], 0, v[64:65]
	v_lshl_add_u64 v[112:113], v[120:121], 0, v[102:103]
	v_lshl_add_u64 v[126:127], v[120:121], 0, v[118:119]
	v_lshl_add_u64 v[90:91], v[88:89], 1, s[14:15]
	v_lshl_add_u64 v[110:111], v[104:105], 1, s[14:15]
	v_lshl_add_u64 v[114:115], v[112:113], 1, s[14:15]
	v_lshl_add_u64 v[126:127], v[126:127], 1, s[14:15]
	s_lshl_b32 s16, s22, 8
	s_ashr_i32 s9, s8, 31
	v_readlane_b32 s21, v255, 7
	s_movk_i32 s20, 0xc0
	v_lshlrev_b32_e32 v131, 3, v153
	v_add_u32_e32 v236, s61, v131
	s_waitcnt vmcnt(22)
	v_pk_add_f32 v[60:61], v[60:61], 1.0 op_sel_hi:[1,0]
	s_waitcnt vmcnt(21)
	v_pk_add_f32 v[66:67], v[66:67], 1.0 op_sel_hi:[1,0]
	s_waitcnt vmcnt(20)
	v_pk_mul_f32 v[134:135], v[70:71], v[60:61]
	v_lshl_add_u64 v[70:71], v[78:79], 0, v[64:65]
	v_pk_add_f32 v[62:63], v[62:63], 1.0 op_sel_hi:[1,0]
	v_pk_add_f32 v[68:69], v[68:69], 1.0 op_sel_hi:[1,0]
	s_waitcnt vmcnt(19)
	v_pk_mul_f32 v[138:139], v[74:75], v[66:67]
	v_lshl_add_u64 v[74:75], v[70:71], 1, s[14:15]
	v_pk_mul_f32 v[132:133], v[72:73], v[62:63]
	v_pk_mul_f32 v[136:137], v[76:77], v[68:69]
	global_load_dwordx4 v[60:63], v[98:99], off offset:64
	global_load_dwordx4 v[66:69], v[98:99], off offset:128
	global_load_dwordx4 v[70:73], v[80:81], off
	s_nop 0
	global_load_dwordx4 v[74:77], v[74:75], off
	v_lshl_add_u64 v[80:81], v[78:79], 0, v[102:103]
	v_lshl_add_u64 v[86:87], v[80:81], 1, s[14:15]
	global_load_dwordx4 v[78:81], v[122:123], off offset:64
	global_load_dwordx4 v[82:85], v[122:123], off offset:128
	s_nop 0
	global_load_dwordx4 v[86:89], v[86:87], off
	s_nop 0
	global_load_dwordx4 v[90:93], v[90:91], off
	s_nop 0
	global_load_dwordx4 v[94:97], v[94:95], off
	s_nop 0
	global_load_dwordx4 v[98:101], v[98:99], off offset:192
	s_nop 0
	global_load_dwordx4 v[102:105], v[106:107], off offset:128
	s_nop 0
	global_load_dwordx4 v[106:109], v[106:107], off offset:192
	s_nop 0
	global_load_dwordx4 v[110:113], v[110:111], off
	s_nop 0
	global_load_dwordx4 v[114:117], v[114:115], off
	s_nop 0
	global_load_dwordx4 v[118:121], v[124:125], off
	s_nop 0
	global_load_dwordx4 v[122:125], v[122:123], off offset:192
	s_waitcnt vmcnt(31)
	v_pk_add_f32 v[140:141], v[156:157], 1.0 op_sel_hi:[1,0]
	global_load_dwordx4 v[126:129], v[126:127], off
	v_pk_mul_f32 v[140:141], v[144:145], v[140:141]
	s_waitcnt vmcnt(29)
	v_pk_add_f32 v[144:145], v[160:161], 1.0 op_sel_hi:[1,0]
	v_pk_add_f32 v[150:151], v[154:155], 1.0 op_sel_hi:[1,0]
	v_pk_mul_f32 v[144:145], v[148:149], v[144:145]
	v_and_or_b32 v148, v222, 48, s16
	s_lshl_b32 s16, s22, 5
	v_lshl_or_b32 v149, v163, 2, s16
	s_lshl_b64 s[16:17], s[66:67], 2
	s_add_u32 s16, s12, s16
	s_addc_u32 s17, s13, s17
	v_readlane_b32 s12, v255, 41
	v_pk_mul_f32 v[142:143], v[142:143], v[150:151]
	v_pk_add_f32 v[150:151], v[158:159], 1.0 op_sel_hi:[1,0]
	v_readlane_b32 s13, v255, 42
	s_add_u32 s18, s10, s12
	v_pk_mul_f32 v[146:147], v[146:147], v[150:151]
	s_addc_u32 s19, s11, s13
	s_movk_i32 s11, 0x810
	v_mov_b32_e32 v151, 0x8100
	v_mad_u32_u24 v151, v162, s11, v151
	v_or_b32_e32 v154, 64, v148
	v_mad_u32_u24 v232, v162, s11, v148
	v_add_u32_e32 v233, v151, v148
	v_mad_u32_u24 v157, v162, s11, v154
	v_add_u32_e32 v158, v154, v151
	v_or_b32_e32 v154, 0x80, v148
	v_or_b32_e32 v148, 0xc0, v148
	v_lshl_add_u32 v156, v162, 2, 0
	v_mad_u32_u24 v159, v162, s11, v154
	v_mad_u32_u24 v161, v162, s11, v148
	v_add_u32_e32 v162, v148, v151
	v_lshlrev_b32_e32 v148, 2, v130
	v_add_u32_e32 v234, 0, v148
	v_add_u32_e32 v235, s21, v148
	v_lshlrev_b32_e32 v148, 3, v222
	v_mul_lo_u32 v64, v130, s20
	v_ashrrev_i32_e32 v150, 2, v130
	s_mul_i32 s10, s22, 0x2040
	v_add_u32_e32 v160, v154, v151
	v_and_b32_e32 v151, 24, v148
	s_load_dwordx2 s[14:15], s[26:27], 0
	s_waitcnt lgkmcnt(0)
	v_add_u32_e32 v231, s21, v64
	v_add_u32_e32 v64, s28, v150
	s_add_i32 s24, s10, 0x810
	s_add_i32 s25, s10, 0x1020
	s_add_i32 s26, s10, 0x1830
	s_add_i32 s27, s10, 0
	s_add_i32 s28, s61, s10
	v_lshl_or_b32 v148, v150, 8, v151
	v_readlane_b32 s10, v255, 8
	v_mul_lo_u32 v163, v149, s20
	s_add_i32 s29, s61, s24
	v_add_u32_e32 v237, s10, v148
	v_lshlrev_b64 v[148:149], 8, v[64:65]
	v_or_b32_e32 v148, v148, v151
	s_mov_b64 s[10:11], 0x300000
	v_lshl_add_u64 v[148:149], v[148:149], 0, s[10:11]
	s_lshl_b64 s[10:11], s[8:9], 15
	s_add_i32 s30, s61, s25
	s_add_i32 s31, s61, s26
	v_lshl_or_b32 v150, v153, 2, s10
	v_mov_b32_e32 v151, s11
	s_lshl_b64 s[10:11], s[8:9], 17
	s_add_u32 s10, s14, s10
	v_mov_b32_e32 v153, v65
	s_addc_u32 s11, s15, s11
	s_lshl_b64 s[8:9], s[8:9], 16
	v_lshl_add_u64 v[152:153], s[10:11], 0, v[152:153]
	v_or_b32_e32 v154, s8, v131
	v_mov_b32_e32 v155, s9
	s_mov_b64 s[20:21], 0
	v_add_u32_e32 v238, v156, v163
	v_add_u32_e32 v239, s61, v157
	v_add_u32_e32 v240, s61, v158
	v_add_u32_e32 v241, s61, v159
	v_add_u32_e32 v242, s61, v160
	v_add_u32_e32 v243, s61, v161
	v_add_u32_e32 v244, s61, v162
	v_mbcnt_lo_u32_b32 v200, -1, 0
	v_mbcnt_hi_u32_b32 v200, -1, v200
	v_lshlrev_b32_e32 v201, 2, v200
	v_cmp_gt_u32_e32 vcc, 4, v200
	s_and_saveexec_b64 s[8:9], vcc
	global_load_dword v202, v201, s[16:17]
	s_or_b64 exec, exec, s[8:9]
	v_cmp_gt_u32_e32 vcc, 32, v200
	s_and_saveexec_b64 s[8:9], vcc
	global_load_dword v203, v201, s[18:19]
	s_or_b64 exec, exec, s[8:9]
	s_waitcnt vmcnt(0)
	v_add_u32_e32 v204, 0x24000, v201
	v_cmp_gt_u32_e32 vcc, 4, v200
	s_and_saveexec_b64 s[8:9], vcc
	ds_write_b32 v204, v202
	s_or_b64 exec, exec, s[8:9]
	v_cmp_gt_u32_e32 vcc, 32, v200
	s_and_saveexec_b64 s[8:9], vcc
	ds_write_b32 v204, v203 offset:16
	s_or_b64 exec, exec, s[8:9]
	s_waitcnt lgkmcnt(0)
	s_branch .LBB0_697

.LBB0_745:
	v_add_co_u32_e32 v172, vcc, 0x6801000, v164
	s_waitcnt vmcnt(15)
	v_cvt_f32_f16_sdwa v227, v175 dst_sel:DWORD dst_unused:UNUSED_PAD src0_sel:WORD_1
	v_cvt_f32_f16_sdwa v247, v174 dst_sel:DWORD dst_unused:UNUSED_PAD src0_sel:WORD_1
	v_cvt_f32_f16_e32 v246, v174
	v_cvt_f32_f16_e32 v226, v175
	v_addc_co_u32_e32 v173, vcc, 0, v165, vcc
	s_waitcnt vmcnt(14)
	v_lshlrev_b32_e32 v224, 16, v212
	v_and_b32_e32 v225, 0xffff0000, v212
	v_add_co_u32_e32 v212, vcc, s74, v164
	v_lshlrev_b32_e32 v174, 16, v213
	v_and_b32_e32 v175, 0xffff0000, v213
	v_addc_co_u32_e32 v213, vcc, 0, v165, vcc
	s_mov_b32 s8, 0x40101000
	v_pk_fma_f32 v[224:225], v[16:17], v[224:225], v[246:247]
	v_pk_fma_f32 v[174:175], v[18:19], v[174:175], v[226:227]
	v_add_co_u32_e32 v164, vcc, s8, v164
	v_cvt_pk_f16_f32 v227, v174, v175
	v_cvt_pk_f16_f32 v226, v224, v225
	v_addc_co_u32_e32 v165, vcc, 0, v165, vcc
	global_store_dwordx2 v[164:165], v[226:227], off offset:-4096 nt
	v_pk_mul_f32 v[226:227], v[174:175], v[174:175]
	v_pk_mul_f32 v[246:247], v[224:225], v[224:225]
	v_cvt_f32_f16_sdwa v251, v208 dst_sel:DWORD dst_unused:UNUSED_PAD src0_sel:WORD_1
	v_pk_mov_b32 v[248:249], v[246:247], v[226:227] op_sel:[1,0]
	v_mov_b32_e32 v247, v227
	v_pk_add_f32 v[226:227], v[248:249], v[246:247]
	v_cvt_f32_f16_sdwa v249, v209 dst_sel:DWORD dst_unused:UNUSED_PAD src0_sel:WORD_1
	v_cvt_f32_f16_e32 v250, v208
	v_cvt_f32_f16_e32 v248, v209
	s_waitcnt vmcnt(14)
	v_lshlrev_b32_e32 v246, 16, v214
	v_and_b32_e32 v247, 0xffff0000, v214
	v_lshlrev_b32_e32 v208, 16, v215
	v_and_b32_e32 v209, 0xffff0000, v215
	v_pk_fma_f32 v[214:215], v[0:1], v[246:247], v[250:251]
	v_pk_fma_f32 v[208:209], v[2:3], v[208:209], v[248:249]
	v_cvt_pk_f16_f32 v246, v214, v215
	v_cvt_pk_f16_f32 v247, v208, v209
	global_store_dwordx2 v[212:213], v[246:247], off offset:512 nt
	v_pk_mul_f32 v[246:247], v[208:209], v[208:209]
	v_pk_mul_f32 v[248:249], v[214:215], v[214:215]
	v_cvt_f32_f16_sdwa v253, v210 dst_sel:DWORD dst_unused:UNUSED_PAD src0_sel:WORD_1
	v_pk_mov_b32 v[250:251], v[248:249], v[246:247] op_sel:[1,0]
	v_mov_b32_e32 v249, v247
	v_pk_add_f32 v[246:247], v[250:251], v[248:249]
	v_cvt_f32_f16_sdwa v251, v211 dst_sel:DWORD dst_unused:UNUSED_PAD src0_sel:WORD_1
	v_cvt_f32_f16_e32 v250, v211
	v_cvt_f32_f16_e32 v252, v210
	s_waitcnt vmcnt(14)
	v_lshlrev_b32_e32 v210, 16, v219
	v_and_b32_e32 v211, 0xffff0000, v219
	v_lshlrev_b32_e32 v248, 16, v218
	v_and_b32_e32 v249, 0xffff0000, v218
	v_pk_fma_f32 v[210:211], v[26:27], v[210:211], v[250:251]
	v_cvt_f32_f16_sdwa v251, v216 dst_sel:DWORD dst_unused:UNUSED_PAD src0_sel:WORD_1
	v_cvt_f32_f16_e32 v250, v216
	v_pk_fma_f32 v[218:219], v[24:25], v[248:249], v[252:253]
	v_cvt_pk_f16_f32 v249, v210, v211
	v_cvt_pk_f16_f32 v248, v218, v219
	global_store_dwordx2 v[212:213], v[248:249], off offset:1024 nt
	s_waitcnt vmcnt(14)
	v_lshlrev_b32_e32 v248, 16, v220
	v_and_b32_e32 v249, 0xffff0000, v220
	v_cvt_f32_f16_sdwa v253, v217 dst_sel:DWORD dst_unused:UNUSED_PAD src0_sel:WORD_1
	v_cvt_f32_f16_e32 v252, v217
	v_lshlrev_b32_e32 v216, 16, v221
	v_and_b32_e32 v217, 0xffff0000, v221
	v_pk_fma_f32 v[220:221], v[28:29], v[248:249], v[250:251]
	v_pk_add_f32 v[226:227], v[226:227], v[226:227] op_sel:[0,1] op_sel_hi:[1,0]
	v_mul_f32_e32 v64, v220, v220
	v_mul_f32_e32 v223, v221, v221
	v_pk_add_f32 v[246:247], v[246:247], v[246:247] op_sel:[0,1] op_sel_hi:[1,0]
	v_mov_b32_e32 v227, v64
	v_mov_b32_e32 v247, v223
	v_mul_f32_e32 v64, v219, v219
	v_pk_fma_f32 v[216:217], v[30:31], v[216:217], v[252:253]
	v_pk_add_f32 v[226:227], v[226:227], v[246:247]
	v_pk_fma_f32 v[246:247], v[218:219], v[218:219], v[64:65] op_sel_hi:[1,1,0]
	v_mul_f32_e32 v64, v211, v211
	v_mul_f32_e32 v245, v216, v216
	v_mul_f32_e32 v248, v217, v217
	v_pk_fma_f32 v[250:251], v[210:211], v[210:211], v[64:65] op_sel_hi:[1,1,0]
	v_mov_b32_e32 v247, v245
	v_mov_b32_e32 v251, v248
	v_pk_add_f32 v[246:247], v[246:247], v[250:251]
	v_cvt_pk_f16_f32 v249, v216, v217
	v_pk_add_f32 v[226:227], v[226:227], v[246:247]
	v_cvt_pk_f16_f32 v248, v220, v221
	v_add_f32_e32 v64, v226, v227
	global_store_dwordx2 v[212:213], v[248:249], off offset:1536 nt
	v_mov_b32_e32 v223, v65
	v_add_f32_dpp v64, v64, v64 quad_perm:[1,0,3,2] row_mask:0xf bank_mask:0xf bound_ctrl:1
	v_lshl_add_u64 v[246:247], s[42:43], 0, v[150:151]
	global_load_dwordx2 v[172:173], v[172:173], off offset:3584
	v_add_f32_dpp v64, v64, v64 quad_perm:[2,3,0,1] row_mask:0xf bank_mask:0xf bound_ctrl:1
	v_mov_b32_e32 v245, v65
	s_nop 0
	v_add_f32_dpp v64, v64, v64 row_half_mirror row_mask:0xf bank_mask:0xf bound_ctrl:1
	s_nop 1
	v_add_f32_dpp v64, v64, v64 row_mirror row_mask:0xf bank_mask:0xf bound_ctrl:1
	s_nop 0
	v_readlane_b32 s10, v64, 16
	v_readlane_b32 s11, v64, 48
	v_readlane_b32 s8, v64, 0
	v_readlane_b32 s9, v64, 32
	v_mov_b32_e32 v226, s10
	v_mov_b32_e32 v227, s11
	v_pk_add_f32 v[226:227], s[8:9], v[226:227]
	s_mov_b32 s8, 0x36800000
	v_add_f32_e32 v64, v226, v227
	v_fmamk_f32 v64, v64, 0x3a800000, v229
	v_rsq_f32_e32 v226, v64
	s_nop 0
	v_pk_mul_f32 v[224:225], v[224:225], v[226:227] op_sel_hi:[1,0]
	v_pk_mul_f32 v[174:175], v[174:175], v[226:227] op_sel_hi:[1,0]
	v_pk_fma_f32 v[224:225], v[134:135], v[224:225], v[4:5]
	v_pk_fma_f32 v[248:249], v[132:133], v[174:175], v[6:7]
	v_med3_f32 v64, v224, s55, v228
	v_med3_f32 v174, v225, s55, v228
	v_cvt_pk_fp8_f32 v223, v64, v174
	v_med3_f32 v64, v248, s55, v228
	v_med3_f32 v174, v249, s55, v228
	v_cvt_pk_bf16_f32 v250, v224, v225
	v_cvt_pk_fp8_f32 v223, v64, v174 op_sel:[0,0,1]
	v_add_co_u32_e32 v174, vcc, s8, v246
	v_cvt_pk_bf16_f32 v251, v248, v249
	s_nop 0
	v_addc_co_u32_e32 v175, vcc, 0, v247, vcc
	v_lshlrev_b32_e32 v246, 16, v250
	v_and_b32_e32 v247, 0xffff0000, v250
	v_pk_add_f32 v[224:225], v[224:225], v[246:247] neg_lo:[0,1] neg_hi:[0,1]
	v_lshlrev_b32_e32 v246, 16, v251
	v_and_b32_e32 v247, 0xffff0000, v251
	v_pk_mul_f32 v[214:215], v[214:215], v[226:227] op_sel_hi:[1,0]
	v_pk_add_f32 v[246:247], v[248:249], v[246:247] neg_lo:[0,1] neg_hi:[0,1]
	v_pk_mul_f32 v[208:209], v[208:209], v[226:227] op_sel_hi:[1,0]
	v_pk_fma_f32 v[214:215], v[138:139], v[214:215], v[8:9]
	v_cvt_pk_bf16_f32 v224, v224, v225
	v_cvt_pk_bf16_f32 v225, v246, v247
	v_pk_fma_f32 v[208:209], v[136:137], v[208:209], v[10:11]
	v_cvt_pk_bf16_f32 v246, v214, v215
	global_store_dword v[174:175], v223, off
	v_med3_f32 v223, v214, s55, v228
	v_med3_f32 v227, v215, s55, v228
	v_cvt_pk_bf16_f32 v247, v208, v209
	v_lshlrev_b32_e32 v248, 16, v246
	v_and_b32_e32 v249, 0xffff0000, v246
	v_cvt_pk_fp8_f32 v245, v223, v227
	v_pk_add_f32 v[214:215], v[214:215], v[248:249] neg_lo:[0,1] neg_hi:[0,1]
	v_lshlrev_b32_e32 v248, 16, v247
	v_and_b32_e32 v249, 0xffff0000, v247
	v_med3_f32 v223, v208, s55, v228
	v_med3_f32 v227, v209, s55, v228
	v_pk_add_f32 v[208:209], v[208:209], v[248:249] neg_lo:[0,1] neg_hi:[0,1]
	v_cvt_pk_bf16_f32 v214, v214, v215
	v_cvt_pk_bf16_f32 v215, v208, v209
	v_pk_mul_f32 v[208:209], v[218:219], v[226:227] op_sel_hi:[1,0]
	v_cvt_pk_fp8_f32 v245, v223, v227 op_sel:[0,0,1]
	v_pk_fma_f32 v[208:209], v[142:143], v[208:209], v[20:21]
	v_pk_mul_f32 v[210:211], v[210:211], v[226:227] op_sel_hi:[1,0]
	v_med3_f32 v218, v208, s55, v228
	v_med3_f32 v219, v209, s55, v228
	v_mov_b32_e32 v227, v65
	v_cvt_pk_fp8_f32 v227, v218, v219
	v_pk_fma_f32 v[210:211], v[140:141], v[210:211], v[22:23]
	v_add_u32_e32 v223, s28, v131
	v_med3_f32 v218, v210, s55, v228
	v_med3_f32 v219, v211, s55, v228
	v_cvt_pk_fp8_f32 v227, v218, v219 op_sel:[0,0,1]
	ds_write2st64_b64 v223, v[224:225], v[214:215] offset1:1
	v_cvt_pk_bf16_f32 v214, v208, v209
	v_cvt_pk_bf16_f32 v215, v210, v211
	v_lshlrev_b32_e32 v218, 16, v214
	v_and_b32_e32 v219, 0xffff0000, v214
	v_pk_add_f32 v[208:209], v[208:209], v[218:219] neg_lo:[0,1] neg_hi:[0,1]
	v_lshlrev_b32_e32 v218, 16, v215
	v_and_b32_e32 v219, 0xffff0000, v215
	v_pk_add_f32 v[210:211], v[210:211], v[218:219] neg_lo:[0,1] neg_hi:[0,1]
	v_pk_mul_f32 v[218:219], v[220:221], v[226:227] op_sel_hi:[1,0]
	v_cvt_pk_bf16_f32 v208, v208, v209
	v_pk_fma_f32 v[218:219], v[146:147], v[218:219], v[12:13]
	v_mov_b32_e32 v221, v65
	v_med3_f32 v209, v218, s55, v228
	v_med3_f32 v220, v219, s55, v228
	v_cvt_pk_fp8_f32 v221, v209, v220
	v_pk_mul_f32 v[216:217], v[216:217], v[226:227] op_sel_hi:[1,0]
	v_add_u32_e32 v64, s27, v131
	v_pk_fma_f32 v[216:217], v[144:145], v[216:217], v[14:15]
	global_store_dword v[174:175], v245, off offset:256
	v_med3_f32 v209, v216, s55, v228
	v_med3_f32 v220, v217, s55, v228
	v_cvt_pk_fp8_f32 v221, v209, v220 op_sel:[0,0,1]
	v_cvt_pk_bf16_f32 v209, v210, v211
	v_cvt_pk_bf16_f32 v210, v218, v219
	v_cvt_pk_bf16_f32 v211, v216, v217
	global_store_dword v[174:175], v221, off offset:768
	v_lshlrev_b32_e32 v220, 16, v210
	v_and_b32_e32 v221, 0xffff0000, v210
	v_pk_add_f32 v[218:219], v[218:219], v[220:221] neg_lo:[0,1] neg_hi:[0,1]
	v_lshlrev_b32_e32 v220, 16, v211
	v_and_b32_e32 v221, 0xffff0000, v211
	v_pk_add_f32 v[216:217], v[216:217], v[220:221] neg_lo:[0,1] neg_hi:[0,1]
	ds_write2st64_b64 v64, v[250:251], v[246:247] offset1:1
	global_store_dword v[174:175], v227, off offset:512
	v_cvt_pk_bf16_f32 v218, v218, v219
	v_cvt_pk_bf16_f32 v219, v216, v217
	ds_write2st64_b64 v64, v[214:215], v[210:211] offset0:2 offset1:3
	ds_write2st64_b64 v223, v[208:209], v[218:219] offset0:2 offset1:3
	v_cvt_f32_f16_sdwa v211, v193 dst_sel:DWORD dst_unused:UNUSED_PAD src0_sel:WORD_1
	v_cvt_f32_f16_sdwa v215, v192 dst_sel:DWORD dst_unused:UNUSED_PAD src0_sel:WORD_1
	v_cvt_f32_f16_e32 v214, v192
	v_cvt_f32_f16_e32 v210, v193
	s_waitcnt vmcnt(19)
	v_lshlrev_b32_e32 v208, 16, v196
	v_and_b32_e32 v209, 0xffff0000, v196
	v_lshlrev_b32_e32 v192, 16, v197
	v_and_b32_e32 v193, 0xffff0000, v197
	v_pk_fma_f32 v[196:197], v[16:17], v[208:209], v[214:215]
	v_pk_fma_f32 v[192:193], v[18:19], v[192:193], v[210:211]
	v_cvt_pk_f16_f32 v208, v196, v197
	v_cvt_pk_f16_f32 v209, v192, v193
	global_store_dwordx2 v[212:213], v[208:209], off offset:2048 nt
	v_pk_mul_f32 v[208:209], v[192:193], v[192:193]
	v_pk_mul_f32 v[210:211], v[196:197], v[196:197]
	v_cvt_f32_f16_sdwa v217, v194 dst_sel:DWORD dst_unused:UNUSED_PAD src0_sel:WORD_1
	v_pk_mov_b32 v[214:215], v[210:211], v[208:209] op_sel:[1,0]
	v_mov_b32_e32 v211, v209
	v_pk_add_f32 v[208:209], v[214:215], v[210:211]
	v_cvt_f32_f16_sdwa v215, v195 dst_sel:DWORD dst_unused:UNUSED_PAD src0_sel:WORD_1
	v_cvt_f32_f16_e32 v216, v194
	v_cvt_f32_f16_e32 v214, v195
	s_waitcnt vmcnt(19)
	v_lshlrev_b32_e32 v210, 16, v200
	v_and_b32_e32 v211, 0xffff0000, v200
	v_lshlrev_b32_e32 v194, 16, v201
	v_and_b32_e32 v195, 0xffff0000, v201
	v_pk_fma_f32 v[200:201], v[0:1], v[210:211], v[216:217]
	v_pk_fma_f32 v[194:195], v[2:3], v[194:195], v[214:215]
	v_cvt_pk_f16_f32 v210, v200, v201
	v_cvt_pk_f16_f32 v211, v194, v195
	v_cvt_f32_f16_sdwa v219, v198 dst_sel:DWORD dst_unused:UNUSED_PAD src0_sel:WORD_1
	v_cvt_f32_f16_e32 v218, v198
	global_store_dwordx2 v[212:213], v[210:211], off offset:2560 nt
	v_pk_mul_f32 v[210:211], v[194:195], v[194:195]
	v_pk_mul_f32 v[214:215], v[200:201], v[200:201]
	s_waitcnt vmcnt(19)
	v_lshlrev_b32_e32 v198, 16, v205
	v_pk_mov_b32 v[216:217], v[214:215], v[210:211] op_sel:[1,0]
	v_mov_b32_e32 v215, v211
	v_pk_add_f32 v[210:211], v[216:217], v[214:215]
	v_lshlrev_b32_e32 v214, 16, v204
	v_and_b32_e32 v215, 0xffff0000, v204
	v_cvt_f32_f16_sdwa v217, v199 dst_sel:DWORD dst_unused:UNUSED_PAD src0_sel:WORD_1
	v_cvt_f32_f16_e32 v216, v199
	v_and_b32_e32 v199, 0xffff0000, v205
	v_pk_fma_f32 v[204:205], v[24:25], v[214:215], v[218:219]
	v_cvt_f32_f16_sdwa v219, v202 dst_sel:DWORD dst_unused:UNUSED_PAD src0_sel:WORD_1
	v_cvt_f32_f16_e32 v218, v202
	v_pk_fma_f32 v[198:199], v[26:27], v[198:199], v[216:217]
	s_waitcnt vmcnt(18)
	v_lshlrev_b32_e32 v216, 16, v206
	v_and_b32_e32 v217, 0xffff0000, v206
	v_cvt_f32_f16_sdwa v221, v203 dst_sel:DWORD dst_unused:UNUSED_PAD src0_sel:WORD_1
	v_cvt_f32_f16_e32 v220, v203
	v_lshlrev_b32_e32 v202, 16, v207
	v_and_b32_e32 v203, 0xffff0000, v207
	v_pk_fma_f32 v[206:207], v[28:29], v[216:217], v[218:219]
	v_pk_add_f32 v[208:209], v[208:209], v[208:209] op_sel:[0,1] op_sel_hi:[1,0]
	v_mul_f32_e32 v216, v206, v206
	v_mul_f32_e32 v217, v207, v207
	v_pk_add_f32 v[210:211], v[210:211], v[210:211] op_sel:[0,1] op_sel_hi:[1,0]
	v_mov_b32_e32 v209, v216
	v_mov_b32_e32 v211, v217
	v_pk_fma_f32 v[202:203], v[30:31], v[202:203], v[220:221]
	v_pk_add_f32 v[208:209], v[208:209], v[210:211]
	v_mul_f32_e32 v210, v205, v205
	v_mul_f32_e32 v216, v199, v199
	v_mul_f32_e32 v218, v202, v202
	v_mul_f32_e32 v219, v203, v203
	v_pk_fma_f32 v[210:211], v[204:205], v[204:205], v[210:211] op_sel_hi:[1,1,0]
	v_pk_fma_f32 v[216:217], v[198:199], v[198:199], v[216:217] op_sel_hi:[1,1,0]
	v_mov_b32_e32 v211, v218
	v_mov_b32_e32 v217, v219
	v_pk_add_f32 v[210:211], v[210:211], v[216:217]
	v_cvt_pk_f16_f32 v215, v198, v199
	v_pk_add_f32 v[208:209], v[208:209], v[210:211]
	v_cvt_pk_f16_f32 v214, v204, v205
	v_add_f32_e32 v208, v208, v209
	global_store_dwordx2 v[212:213], v[214:215], off offset:3072 nt
	v_mov_b32_e32 v215, v65
	v_add_f32_dpp v208, v208, v208 quad_perm:[1,0,3,2] row_mask:0xf bank_mask:0xf bound_ctrl:1
	v_cvt_pk_f16_f32 v211, v202, v203
	v_cvt_pk_f16_f32 v210, v206, v207
	v_add_f32_dpp v208, v208, v208 quad_perm:[2,3,0,1] row_mask:0xf bank_mask:0xf bound_ctrl:1
	global_store_dwordx2 v[212:213], v[210:211], off offset:3584 nt
	s_nop 0
	v_add_f32_dpp v208, v208, v208 row_half_mirror row_mask:0xf bank_mask:0xf bound_ctrl:1
	s_nop 1
	v_add_f32_dpp v208, v208, v208 row_mirror row_mask:0xf bank_mask:0xf bound_ctrl:1
	s_nop 0
	v_readlane_b32 s10, v208, 16
	v_readlane_b32 s11, v208, 48
	v_readlane_b32 s8, v208, 0
	v_readlane_b32 s9, v208, 32
	v_mov_b32_e32 v208, s10
	v_mov_b32_e32 v209, s11
	v_pk_add_f32 v[208:209], s[8:9], v[208:209]
	s_nop 0
	v_add_f32_e32 v208, v208, v209
	v_fmamk_f32 v208, v208, 0x3a800000, v229
	v_rsq_f32_e32 v208, v208
	s_nop 0
	v_pk_mul_f32 v[196:197], v[196:197], v[208:209] op_sel_hi:[1,0]
	s_nop 0
	v_pk_fma_f32 v[196:197], v[134:135], v[196:197], v[4:5]
	v_pk_mul_f32 v[192:193], v[192:193], v[208:209] op_sel_hi:[1,0]
	v_med3_f32 v209, v196, s55, v228
	v_med3_f32 v214, v197, s55, v228
	v_cvt_pk_fp8_f32 v215, v209, v214
	v_pk_fma_f32 v[192:193], v[132:133], v[192:193], v[6:7]
	v_cvt_pk_bf16_f32 v210, v196, v197
	v_cvt_pk_bf16_f32 v211, v192, v193
	v_lshlrev_b32_e32 v212, 16, v210
	v_and_b32_e32 v213, 0xffff0000, v210
	v_med3_f32 v209, v192, s55, v228
	v_med3_f32 v214, v193, s55, v228
	v_pk_add_f32 v[196:197], v[196:197], v[212:213] neg_lo:[0,1] neg_hi:[0,1]
	v_lshlrev_b32_e32 v212, 16, v211
	v_and_b32_e32 v213, 0xffff0000, v211
	v_cvt_pk_fp8_f32 v215, v209, v214 op_sel:[0,0,1]
	v_pk_add_f32 v[192:193], v[192:193], v[212:213] neg_lo:[0,1] neg_hi:[0,1]
	v_add_u32_e32 v209, s24, v236
	v_cvt_pk_bf16_f32 v196, v196, v197
	v_cvt_pk_bf16_f32 v197, v192, v193
	v_pk_mul_f32 v[192:193], v[200:201], v[208:209] op_sel_hi:[1,0]
	v_mov_b32_e32 v212, v65
	v_pk_fma_f32 v[192:193], v[138:139], v[192:193], v[8:9]
	v_pk_mul_f32 v[194:195], v[194:195], v[208:209] op_sel_hi:[1,0]
	v_med3_f32 v200, v192, s55, v228
	v_med3_f32 v201, v193, s55, v228
	v_cvt_pk_fp8_f32 v212, v200, v201
	v_pk_fma_f32 v[194:195], v[136:137], v[194:195], v[10:11]
	ds_write_b64 v209, v[196:197]
	v_med3_f32 v200, v194, s55, v228
	v_med3_f32 v201, v195, s55, v228
	v_cvt_pk_bf16_f32 v196, v192, v193
	v_cvt_pk_fp8_f32 v212, v200, v201 op_sel:[0,0,1]
	v_cvt_pk_bf16_f32 v197, v194, v195
	v_lshlrev_b32_e32 v200, 16, v196
	v_and_b32_e32 v201, 0xffff0000, v196
	v_pk_add_f32 v[192:193], v[192:193], v[200:201] neg_lo:[0,1] neg_hi:[0,1]
	v_lshlrev_b32_e32 v200, 16, v197
	v_and_b32_e32 v201, 0xffff0000, v197
	v_pk_add_f32 v[194:195], v[194:195], v[200:201] neg_lo:[0,1] neg_hi:[0,1]
	v_add_u32_e32 v209, 16, v64
	v_cvt_pk_bf16_f32 v192, v192, v193
	v_cvt_pk_bf16_f32 v193, v194, v195
	v_pk_mul_f32 v[194:195], v[204:205], v[208:209] op_sel_hi:[1,0]
	ds_write2st64_b64 v209, v[210:211], v[196:197] offset0:4 offset1:5
	v_pk_fma_f32 v[194:195], v[142:143], v[194:195], v[20:21]
	v_pk_mul_f32 v[196:197], v[198:199], v[208:209] op_sel_hi:[1,0]
	v_med3_f32 v198, v194, s55, v228
	v_med3_f32 v199, v195, s55, v228
	v_mov_b32_e32 v200, v65
	v_cvt_pk_fp8_f32 v200, v198, v199
	v_pk_fma_f32 v[196:197], v[140:141], v[196:197], v[22:23]
	v_mov_b32_e32 v205, v65
	v_med3_f32 v198, v196, s55, v228
	v_med3_f32 v199, v197, s55, v228
	v_cvt_pk_fp8_f32 v200, v198, v199 op_sel:[0,0,1]
	v_cvt_pk_bf16_f32 v198, v194, v195
	v_cvt_pk_bf16_f32 v199, v196, v197
	v_and_b32_e32 v201, 0xffff0000, v198
	global_store_dword v[174:175], v200, off offset:1536
	v_lshlrev_b32_e32 v200, 16, v198
	v_pk_add_f32 v[194:195], v[194:195], v[200:201] neg_lo:[0,1] neg_hi:[0,1]
	v_lshlrev_b32_e32 v200, 16, v199
	v_and_b32_e32 v201, 0xffff0000, v199
	v_pk_add_f32 v[196:197], v[196:197], v[200:201] neg_lo:[0,1] neg_hi:[0,1]
	v_cvt_pk_bf16_f32 v194, v194, v195
	v_cvt_pk_bf16_f32 v195, v196, v197
	v_pk_mul_f32 v[196:197], v[206:207], v[208:209] op_sel_hi:[1,0]
	v_pk_mul_f32 v[200:201], v[202:203], v[208:209] op_sel_hi:[1,0]
	v_pk_fma_f32 v[196:197], v[146:147], v[196:197], v[12:13]
	v_add_u32_e32 v204, s29, v131
	v_med3_f32 v202, v196, s55, v228
	v_med3_f32 v203, v197, s55, v228
	v_cvt_pk_fp8_f32 v205, v202, v203
	v_pk_fma_f32 v[200:201], v[144:145], v[200:201], v[14:15]
	ds_write2st64_b64 v204, v[192:193], v[194:195] offset0:1 offset1:2
	v_med3_f32 v202, v200, s55, v228
	v_med3_f32 v203, v201, s55, v228
	v_cvt_pk_bf16_f32 v192, v196, v197
	v_cvt_pk_fp8_f32 v205, v202, v203 op_sel:[0,0,1]
	v_cvt_pk_bf16_f32 v193, v200, v201
	v_lshlrev_b32_e32 v194, 16, v192
	v_and_b32_e32 v195, 0xffff0000, v192
	v_pk_add_f32 v[194:195], v[196:197], v[194:195] neg_lo:[0,1] neg_hi:[0,1]
	v_lshlrev_b32_e32 v196, 16, v193
	v_and_b32_e32 v197, 0xffff0000, v193
	v_pk_add_f32 v[196:197], v[200:201], v[196:197] neg_lo:[0,1] neg_hi:[0,1]
	v_cvt_pk_bf16_f32 v194, v194, v195
	v_cvt_pk_bf16_f32 v195, v196, v197
	global_store_dword v[174:175], v215, off offset:1024
	global_store_dword v[174:175], v212, off offset:1280
	global_store_dword v[174:175], v205, off offset:1792
	ds_write2st64_b64 v209, v[198:199], v[192:193] offset0:6 offset1:7
	ds_write_b64 v204, v[194:195] offset:1536
	v_cvt_f32_f16_sdwa v195, v177 dst_sel:DWORD dst_unused:UNUSED_PAD src0_sel:WORD_1
	v_cvt_f32_f16_sdwa v197, v176 dst_sel:DWORD dst_unused:UNUSED_PAD src0_sel:WORD_1
	v_cvt_f32_f16_e32 v196, v176
	v_cvt_f32_f16_e32 v194, v177
	s_waitcnt vmcnt(23)
	v_lshlrev_b32_e32 v192, 16, v180
	v_and_b32_e32 v193, 0xffff0000, v180
	v_lshlrev_b32_e32 v176, 16, v181
	v_and_b32_e32 v177, 0xffff0000, v181
	v_pk_fma_f32 v[180:181], v[16:17], v[192:193], v[196:197]
	v_pk_fma_f32 v[176:177], v[18:19], v[176:177], v[194:195]
	v_cvt_pk_f16_f32 v192, v180, v181
	v_cvt_pk_f16_f32 v193, v176, v177
	global_store_dwordx2 v[164:165], v[192:193], off nt
	v_pk_mul_f32 v[192:193], v[176:177], v[176:177]
	v_pk_mul_f32 v[194:195], v[180:181], v[180:181]
	v_cvt_f32_f16_sdwa v199, v178 dst_sel:DWORD dst_unused:UNUSED_PAD src0_sel:WORD_1
	v_pk_mov_b32 v[196:197], v[194:195], v[192:193] op_sel:[1,0]
	v_mov_b32_e32 v195, v193
	v_pk_add_f32 v[192:193], v[196:197], v[194:195]
	v_cvt_f32_f16_sdwa v197, v179 dst_sel:DWORD dst_unused:UNUSED_PAD src0_sel:WORD_1
	v_cvt_f32_f16_e32 v198, v178
	v_cvt_f32_f16_e32 v196, v179
	s_waitcnt vmcnt(23)
	v_lshlrev_b32_e32 v194, 16, v184
	v_and_b32_e32 v195, 0xffff0000, v184
	v_lshlrev_b32_e32 v178, 16, v185
	v_and_b32_e32 v179, 0xffff0000, v185
	v_pk_fma_f32 v[184:185], v[0:1], v[194:195], v[198:199]
	v_pk_fma_f32 v[178:179], v[2:3], v[178:179], v[196:197]
	v_cvt_pk_f16_f32 v194, v184, v185
	v_cvt_pk_f16_f32 v195, v178, v179
	v_cvt_f32_f16_sdwa v201, v182 dst_sel:DWORD dst_unused:UNUSED_PAD src0_sel:WORD_1
	v_cvt_f32_f16_e32 v200, v182
	global_store_dwordx2 v[164:165], v[194:195], off offset:512 nt
	v_pk_mul_f32 v[194:195], v[178:179], v[178:179]
	v_pk_mul_f32 v[196:197], v[184:185], v[184:185]
	s_waitcnt vmcnt(23)
	v_lshlrev_b32_e32 v182, 16, v189
	v_pk_mov_b32 v[198:199], v[196:197], v[194:195] op_sel:[1,0]
	v_mov_b32_e32 v197, v195
	v_pk_add_f32 v[194:195], v[198:199], v[196:197]
	v_lshlrev_b32_e32 v196, 16, v188
	v_and_b32_e32 v197, 0xffff0000, v188
	v_cvt_f32_f16_sdwa v199, v183 dst_sel:DWORD dst_unused:UNUSED_PAD src0_sel:WORD_1
	v_cvt_f32_f16_e32 v198, v183
	v_and_b32_e32 v183, 0xffff0000, v189
	v_pk_fma_f32 v[188:189], v[24:25], v[196:197], v[200:201]
	v_cvt_f32_f16_sdwa v201, v186 dst_sel:DWORD dst_unused:UNUSED_PAD src0_sel:WORD_1
	v_cvt_f32_f16_e32 v200, v186
	v_pk_fma_f32 v[182:183], v[26:27], v[182:183], v[198:199]
	s_waitcnt vmcnt(22)
	v_lshlrev_b32_e32 v198, 16, v190
	v_and_b32_e32 v199, 0xffff0000, v190
	v_cvt_f32_f16_sdwa v203, v187 dst_sel:DWORD dst_unused:UNUSED_PAD src0_sel:WORD_1
	v_cvt_f32_f16_e32 v202, v187
	v_lshlrev_b32_e32 v186, 16, v191
	v_and_b32_e32 v187, 0xffff0000, v191
	v_pk_fma_f32 v[190:191], v[28:29], v[198:199], v[200:201]
	v_pk_add_f32 v[192:193], v[192:193], v[192:193] op_sel:[0,1] op_sel_hi:[1,0]
	v_mul_f32_e32 v198, v190, v190
	v_mul_f32_e32 v199, v191, v191
	v_pk_add_f32 v[194:195], v[194:195], v[194:195] op_sel:[0,1] op_sel_hi:[1,0]
	v_mov_b32_e32 v193, v198
	v_mov_b32_e32 v195, v199
	v_pk_fma_f32 v[186:187], v[30:31], v[186:187], v[202:203]
	v_pk_add_f32 v[192:193], v[192:193], v[194:195]
	v_mul_f32_e32 v194, v189, v189
	v_mul_f32_e32 v198, v183, v183
	v_mul_f32_e32 v200, v186, v186
	v_mul_f32_e32 v201, v187, v187
	v_pk_fma_f32 v[194:195], v[188:189], v[188:189], v[194:195] op_sel_hi:[1,1,0]
	v_pk_fma_f32 v[198:199], v[182:183], v[182:183], v[198:199] op_sel_hi:[1,1,0]
	v_mov_b32_e32 v195, v200
	v_mov_b32_e32 v199, v201
	v_pk_add_f32 v[194:195], v[194:195], v[198:199]
	v_cvt_pk_f16_f32 v197, v182, v183
	v_pk_add_f32 v[192:193], v[192:193], v[194:195]
	v_cvt_pk_f16_f32 v196, v188, v189
	v_add_f32_e32 v192, v192, v193
	global_store_dwordx2 v[164:165], v[196:197], off offset:1024 nt
	v_mov_b32_e32 v197, v65
	v_add_f32_dpp v192, v192, v192 quad_perm:[1,0,3,2] row_mask:0xf bank_mask:0xf bound_ctrl:1
	v_cvt_pk_f16_f32 v195, v186, v187
	v_cvt_pk_f16_f32 v194, v190, v191
	v_add_f32_dpp v192, v192, v192 quad_perm:[2,3,0,1] row_mask:0xf bank_mask:0xf bound_ctrl:1
	global_store_dwordx2 v[164:165], v[194:195], off offset:1536 nt
	s_nop 0
	v_add_f32_dpp v192, v192, v192 row_half_mirror row_mask:0xf bank_mask:0xf bound_ctrl:1
	s_nop 1
	v_add_f32_dpp v192, v192, v192 row_mirror row_mask:0xf bank_mask:0xf bound_ctrl:1
	s_nop 0
	v_readlane_b32 s10, v192, 16
	v_readlane_b32 s11, v192, 48
	v_readlane_b32 s8, v192, 0
	v_readlane_b32 s9, v192, 32
	v_mov_b32_e32 v192, s10
	v_mov_b32_e32 v193, s11
	v_pk_add_f32 v[192:193], s[8:9], v[192:193]
	s_nop 0
	v_add_f32_e32 v192, v192, v193
	v_fmamk_f32 v192, v192, 0x3a800000, v229
	v_rsq_f32_e32 v192, v192
	s_nop 0
	v_pk_mul_f32 v[180:181], v[180:181], v[192:193] op_sel_hi:[1,0]
	s_nop 0
	v_pk_fma_f32 v[180:181], v[134:135], v[180:181], v[4:5]
	v_pk_mul_f32 v[176:177], v[176:177], v[192:193] op_sel_hi:[1,0]
	v_med3_f32 v193, v180, s55, v228
	v_med3_f32 v196, v181, s55, v228
	v_cvt_pk_fp8_f32 v197, v193, v196
	v_pk_fma_f32 v[176:177], v[132:133], v[176:177], v[6:7]
	v_cvt_pk_bf16_f32 v194, v180, v181
	v_med3_f32 v193, v176, s55, v228
	v_med3_f32 v196, v177, s55, v228
	v_cvt_pk_fp8_f32 v197, v193, v196 op_sel:[0,0,1]
	v_cvt_pk_bf16_f32 v195, v176, v177
	v_lshlrev_b32_e32 v196, 16, v194
	v_add_u32_e32 v193, s25, v236
	global_store_dword v[174:175], v197, off offset:2048
	v_and_b32_e32 v197, 0xffff0000, v194
	v_pk_add_f32 v[180:181], v[180:181], v[196:197] neg_lo:[0,1] neg_hi:[0,1]
	v_lshlrev_b32_e32 v196, 16, v195
	v_and_b32_e32 v197, 0xffff0000, v195
	v_pk_add_f32 v[176:177], v[176:177], v[196:197] neg_lo:[0,1] neg_hi:[0,1]
	v_cvt_pk_bf16_f32 v180, v180, v181
	v_cvt_pk_bf16_f32 v181, v176, v177
	v_pk_mul_f32 v[176:177], v[184:185], v[192:193] op_sel_hi:[1,0]
	v_mov_b32_e32 v196, v65
	v_pk_fma_f32 v[176:177], v[138:139], v[176:177], v[8:9]
	v_pk_mul_f32 v[178:179], v[178:179], v[192:193] op_sel_hi:[1,0]
	v_med3_f32 v184, v176, s55, v228
	v_med3_f32 v185, v177, s55, v228
	v_cvt_pk_fp8_f32 v196, v184, v185
	v_pk_fma_f32 v[178:179], v[136:137], v[178:179], v[10:11]
	ds_write_b64 v193, v[180:181]
	v_med3_f32 v184, v178, s55, v228
	v_med3_f32 v185, v179, s55, v228
	v_cvt_pk_bf16_f32 v180, v176, v177
	v_cvt_pk_fp8_f32 v196, v184, v185 op_sel:[0,0,1]
	v_cvt_pk_bf16_f32 v181, v178, v179
	v_lshlrev_b32_e32 v184, 16, v180
	v_and_b32_e32 v185, 0xffff0000, v180
	v_pk_add_f32 v[176:177], v[176:177], v[184:185] neg_lo:[0,1] neg_hi:[0,1]
	v_lshlrev_b32_e32 v184, 16, v181
	v_and_b32_e32 v185, 0xffff0000, v181
	v_pk_add_f32 v[178:179], v[178:179], v[184:185] neg_lo:[0,1] neg_hi:[0,1]
	v_add_u32_e32 v193, 32, v64
	v_cvt_pk_bf16_f32 v176, v176, v177
	v_cvt_pk_bf16_f32 v177, v178, v179
	v_pk_mul_f32 v[178:179], v[188:189], v[192:193] op_sel_hi:[1,0]
	ds_write2st64_b64 v193, v[194:195], v[180:181] offset0:8 offset1:9
	v_pk_fma_f32 v[178:179], v[142:143], v[178:179], v[20:21]
	v_pk_mul_f32 v[180:181], v[182:183], v[192:193] op_sel_hi:[1,0]
	v_med3_f32 v182, v178, s55, v228
	v_med3_f32 v183, v179, s55, v228
	v_mov_b32_e32 v184, v65
	v_cvt_pk_fp8_f32 v184, v182, v183
	v_pk_fma_f32 v[180:181], v[140:141], v[180:181], v[22:23]
	v_mov_b32_e32 v189, v65
	v_med3_f32 v182, v180, s55, v228
	v_med3_f32 v183, v181, s55, v228
	v_cvt_pk_fp8_f32 v184, v182, v183 op_sel:[0,0,1]
	v_cvt_pk_bf16_f32 v182, v178, v179
	v_cvt_pk_bf16_f32 v183, v180, v181
	v_and_b32_e32 v185, 0xffff0000, v182
	global_store_dword v[174:175], v184, off offset:2560
	v_lshlrev_b32_e32 v184, 16, v182
	v_pk_add_f32 v[178:179], v[178:179], v[184:185] neg_lo:[0,1] neg_hi:[0,1]
	v_lshlrev_b32_e32 v184, 16, v183
	v_and_b32_e32 v185, 0xffff0000, v183
	v_pk_add_f32 v[180:181], v[180:181], v[184:185] neg_lo:[0,1] neg_hi:[0,1]
	v_cvt_pk_bf16_f32 v178, v178, v179
	v_cvt_pk_bf16_f32 v179, v180, v181
	v_pk_mul_f32 v[180:181], v[190:191], v[192:193] op_sel_hi:[1,0]
	v_pk_mul_f32 v[184:185], v[186:187], v[192:193] op_sel_hi:[1,0]
	v_pk_fma_f32 v[180:181], v[146:147], v[180:181], v[12:13]
	v_add_u32_e32 v188, s30, v131
	v_med3_f32 v186, v180, s55, v228
	v_med3_f32 v187, v181, s55, v228
	v_cvt_pk_fp8_f32 v189, v186, v187
	v_pk_fma_f32 v[184:185], v[144:145], v[184:185], v[14:15]
	ds_write2st64_b64 v188, v[176:177], v[178:179] offset0:1 offset1:2
	v_med3_f32 v186, v184, s55, v228
	v_med3_f32 v187, v185, s55, v228
	v_cvt_pk_bf16_f32 v176, v180, v181
	v_cvt_pk_fp8_f32 v189, v186, v187 op_sel:[0,0,1]
	v_cvt_pk_bf16_f32 v177, v184, v185
	v_lshlrev_b32_e32 v178, 16, v176
	v_and_b32_e32 v179, 0xffff0000, v176
	v_pk_add_f32 v[178:179], v[180:181], v[178:179] neg_lo:[0,1] neg_hi:[0,1]
	v_lshlrev_b32_e32 v180, 16, v177
	v_and_b32_e32 v181, 0xffff0000, v177
	v_pk_add_f32 v[180:181], v[184:185], v[180:181] neg_lo:[0,1] neg_hi:[0,1]
	v_cvt_pk_bf16_f32 v178, v178, v179
	v_cvt_pk_bf16_f32 v179, v180, v181
	global_store_dword v[174:175], v196, off offset:2304
	global_store_dword v[174:175], v189, off offset:2816
	ds_write2st64_b64 v193, v[182:183], v[176:177] offset0:10 offset1:11
	ds_write_b64 v188, v[178:179] offset:1536
	v_cvt_f32_f16_sdwa v179, v157 dst_sel:DWORD dst_unused:UNUSED_PAD src0_sel:WORD_1
	v_cvt_f32_f16_sdwa v181, v156 dst_sel:DWORD dst_unused:UNUSED_PAD src0_sel:WORD_1
	v_cvt_f32_f16_e32 v180, v156
	v_cvt_f32_f16_e32 v178, v157
	s_waitcnt vmcnt(27)
	v_lshlrev_b32_e32 v176, 16, v160
	v_and_b32_e32 v177, 0xffff0000, v160
	v_lshlrev_b32_e32 v156, 16, v161
	v_and_b32_e32 v157, 0xffff0000, v161
	v_pk_fma_f32 v[160:161], v[16:17], v[176:177], v[180:181]
	v_pk_fma_f32 v[156:157], v[18:19], v[156:157], v[178:179]
	v_cvt_pk_f16_f32 v176, v160, v161
	v_cvt_pk_f16_f32 v177, v156, v157
	global_store_dwordx2 v[164:165], v[176:177], off offset:2048 nt
	v_pk_mul_f32 v[176:177], v[156:157], v[156:157]
	v_pk_mul_f32 v[178:179], v[160:161], v[160:161]
	v_cvt_f32_f16_sdwa v183, v158 dst_sel:DWORD dst_unused:UNUSED_PAD src0_sel:WORD_1
	v_pk_mov_b32 v[180:181], v[178:179], v[176:177] op_sel:[1,0]
	v_mov_b32_e32 v179, v177
	v_pk_add_f32 v[176:177], v[180:181], v[178:179]
	v_cvt_f32_f16_sdwa v181, v159 dst_sel:DWORD dst_unused:UNUSED_PAD src0_sel:WORD_1
	v_cvt_f32_f16_e32 v182, v158
	v_cvt_f32_f16_e32 v180, v159
	s_waitcnt vmcnt(27)
	v_lshlrev_b32_e32 v178, 16, v166
	v_and_b32_e32 v179, 0xffff0000, v166
	v_lshlrev_b32_e32 v158, 16, v167
	v_and_b32_e32 v159, 0xffff0000, v167
	v_pk_fma_f32 v[166:167], v[0:1], v[178:179], v[182:183]
	v_pk_fma_f32 v[158:159], v[2:3], v[158:159], v[180:181]
	v_cvt_pk_f16_f32 v178, v166, v167
	v_cvt_pk_f16_f32 v179, v158, v159
	v_cvt_f32_f16_sdwa v185, v162 dst_sel:DWORD dst_unused:UNUSED_PAD src0_sel:WORD_1
	v_cvt_f32_f16_e32 v184, v162
	global_store_dwordx2 v[164:165], v[178:179], off offset:2560 nt
	v_pk_mul_f32 v[178:179], v[158:159], v[158:159]
	v_pk_mul_f32 v[180:181], v[166:167], v[166:167]
	s_waitcnt vmcnt(27)
	v_lshlrev_b32_e32 v162, 16, v171
	v_pk_mov_b32 v[182:183], v[180:181], v[178:179] op_sel:[1,0]
	v_mov_b32_e32 v181, v179
	v_pk_add_f32 v[178:179], v[182:183], v[180:181]
	v_lshlrev_b32_e32 v180, 16, v170
	v_and_b32_e32 v181, 0xffff0000, v170
	v_cvt_f32_f16_sdwa v183, v163 dst_sel:DWORD dst_unused:UNUSED_PAD src0_sel:WORD_1
	v_cvt_f32_f16_e32 v182, v163
	v_and_b32_e32 v163, 0xffff0000, v171
	v_pk_fma_f32 v[170:171], v[24:25], v[180:181], v[184:185]
	v_cvt_f32_f16_sdwa v185, v168 dst_sel:DWORD dst_unused:UNUSED_PAD src0_sel:WORD_1
	v_cvt_f32_f16_e32 v184, v168
	v_pk_fma_f32 v[162:163], v[26:27], v[162:163], v[182:183]
	s_waitcnt vmcnt(22)
	v_lshlrev_b32_e32 v182, 16, v172
	v_and_b32_e32 v183, 0xffff0000, v172
	v_cvt_f32_f16_sdwa v187, v169 dst_sel:DWORD dst_unused:UNUSED_PAD src0_sel:WORD_1
	v_cvt_f32_f16_e32 v186, v169
	v_lshlrev_b32_e32 v168, 16, v173
	v_and_b32_e32 v169, 0xffff0000, v173
	v_pk_fma_f32 v[172:173], v[28:29], v[182:183], v[184:185]
	v_pk_add_f32 v[176:177], v[176:177], v[176:177] op_sel:[0,1] op_sel_hi:[1,0]
	v_mul_f32_e32 v182, v172, v172
	v_mul_f32_e32 v183, v173, v173
	v_pk_add_f32 v[178:179], v[178:179], v[178:179] op_sel:[0,1] op_sel_hi:[1,0]
	v_mov_b32_e32 v177, v182
	v_mov_b32_e32 v179, v183
	v_pk_fma_f32 v[168:169], v[30:31], v[168:169], v[186:187]
	v_pk_add_f32 v[176:177], v[176:177], v[178:179]
	v_mul_f32_e32 v178, v171, v171
	v_mul_f32_e32 v182, v163, v163
	v_mul_f32_e32 v184, v168, v168
	v_mul_f32_e32 v185, v169, v169
	v_pk_fma_f32 v[178:179], v[170:171], v[170:171], v[178:179] op_sel_hi:[1,1,0]
	v_pk_fma_f32 v[182:183], v[162:163], v[162:163], v[182:183] op_sel_hi:[1,1,0]
	v_mov_b32_e32 v179, v184
	v_mov_b32_e32 v183, v185
	v_pk_add_f32 v[178:179], v[178:179], v[182:183]
	v_cvt_pk_f16_f32 v181, v162, v163
	v_pk_add_f32 v[176:177], v[176:177], v[178:179]
	v_cvt_pk_f16_f32 v180, v170, v171
	v_add_f32_e32 v176, v176, v177
	global_store_dwordx2 v[164:165], v[180:181], off offset:3072 nt
	v_mov_b32_e32 v181, v65
	v_add_f32_dpp v176, v176, v176 quad_perm:[1,0,3,2] row_mask:0xf bank_mask:0xf bound_ctrl:1
	v_cvt_pk_f16_f32 v179, v168, v169
	v_cvt_pk_f16_f32 v178, v172, v173
	v_add_f32_dpp v176, v176, v176 quad_perm:[2,3,0,1] row_mask:0xf bank_mask:0xf bound_ctrl:1
	global_store_dwordx2 v[164:165], v[178:179], off offset:3584 nt
	v_add_u32_e32 v64, 48, v64
	v_add_f32_dpp v176, v176, v176 row_half_mirror row_mask:0xf bank_mask:0xf bound_ctrl:1
	s_nop 1
	v_add_f32_dpp v176, v176, v176 row_mirror row_mask:0xf bank_mask:0xf bound_ctrl:1
	s_nop 0
	v_readlane_b32 s10, v176, 16
	v_readlane_b32 s11, v176, 48
	v_readlane_b32 s8, v176, 0
	v_readlane_b32 s9, v176, 32
	v_mov_b32_e32 v176, s10
	v_mov_b32_e32 v177, s11
	v_pk_add_f32 v[176:177], s[8:9], v[176:177]
	s_nop 0
	v_add_f32_e32 v176, v176, v177
	v_fmamk_f32 v176, v176, 0x3a800000, v229
	v_rsq_f32_e32 v176, v176
	s_nop 0
	v_pk_mul_f32 v[160:161], v[160:161], v[176:177] op_sel_hi:[1,0]
	s_nop 0
	v_pk_fma_f32 v[160:161], v[134:135], v[160:161], v[4:5]
	v_pk_mul_f32 v[156:157], v[156:157], v[176:177] op_sel_hi:[1,0]
	v_med3_f32 v177, v160, s55, v228
	v_med3_f32 v180, v161, s55, v228
	v_cvt_pk_fp8_f32 v181, v177, v180
	v_pk_fma_f32 v[156:157], v[132:133], v[156:157], v[6:7]
	v_cvt_pk_bf16_f32 v164, v160, v161
	v_cvt_pk_bf16_f32 v165, v156, v157
	v_lshlrev_b32_e32 v178, 16, v164
	v_and_b32_e32 v179, 0xffff0000, v164
	v_med3_f32 v177, v156, s55, v228
	v_med3_f32 v180, v157, s55, v228
	v_pk_add_f32 v[160:161], v[160:161], v[178:179] neg_lo:[0,1] neg_hi:[0,1]
	v_lshlrev_b32_e32 v178, 16, v165
	v_and_b32_e32 v179, 0xffff0000, v165
	v_cvt_pk_fp8_f32 v181, v177, v180 op_sel:[0,0,1]
	v_pk_add_f32 v[156:157], v[156:157], v[178:179] neg_lo:[0,1] neg_hi:[0,1]
	v_add_u32_e32 v177, s26, v236
	v_cvt_pk_bf16_f32 v160, v160, v161
	v_cvt_pk_bf16_f32 v161, v156, v157
	v_pk_mul_f32 v[156:157], v[166:167], v[176:177] op_sel_hi:[1,0]
	v_mov_b32_e32 v178, v65
	v_pk_fma_f32 v[156:157], v[138:139], v[156:157], v[8:9]
	v_pk_mul_f32 v[158:159], v[158:159], v[176:177] op_sel_hi:[1,0]
	v_med3_f32 v166, v156, s55, v228
	v_med3_f32 v167, v157, s55, v228
	v_cvt_pk_fp8_f32 v178, v166, v167
	v_pk_fma_f32 v[158:159], v[136:137], v[158:159], v[10:11]
	ds_write_b64 v177, v[160:161]
	v_med3_f32 v166, v158, s55, v228
	v_med3_f32 v167, v159, s55, v228
	v_cvt_pk_bf16_f32 v160, v156, v157
	v_cvt_pk_fp8_f32 v178, v166, v167 op_sel:[0,0,1]
	v_cvt_pk_bf16_f32 v161, v158, v159
	v_lshlrev_b32_e32 v166, 16, v160
	v_and_b32_e32 v167, 0xffff0000, v160
	v_pk_add_f32 v[156:157], v[156:157], v[166:167] neg_lo:[0,1] neg_hi:[0,1]
	v_lshlrev_b32_e32 v166, 16, v161
	v_and_b32_e32 v167, 0xffff0000, v161
	v_pk_add_f32 v[158:159], v[158:159], v[166:167] neg_lo:[0,1] neg_hi:[0,1]
	v_cvt_pk_bf16_f32 v156, v156, v157
	v_cvt_pk_bf16_f32 v157, v158, v159
	v_pk_mul_f32 v[158:159], v[170:171], v[176:177] op_sel_hi:[1,0]
	ds_write2st64_b64 v64, v[164:165], v[160:161] offset0:12 offset1:13
	v_pk_fma_f32 v[158:159], v[142:143], v[158:159], v[20:21]
	v_pk_mul_f32 v[160:161], v[162:163], v[176:177] op_sel_hi:[1,0]
	v_med3_f32 v162, v158, s55, v228
	v_med3_f32 v163, v159, s55, v228
	v_mov_b32_e32 v164, v65
	v_cvt_pk_fp8_f32 v164, v162, v163
	v_pk_fma_f32 v[160:161], v[140:141], v[160:161], v[22:23]
	v_add_u32_e32 v166, s31, v131
	v_med3_f32 v162, v160, s55, v228
	v_med3_f32 v163, v161, s55, v228
	v_cvt_pk_fp8_f32 v164, v162, v163 op_sel:[0,0,1]
	v_cvt_pk_bf16_f32 v162, v158, v159
	v_cvt_pk_bf16_f32 v163, v160, v161
	v_and_b32_e32 v165, 0xffff0000, v162
	global_store_dword v[174:175], v164, off offset:3584
	v_lshlrev_b32_e32 v164, 16, v162
	v_pk_add_f32 v[158:159], v[158:159], v[164:165] neg_lo:[0,1] neg_hi:[0,1]
	v_lshlrev_b32_e32 v164, 16, v163
	v_and_b32_e32 v165, 0xffff0000, v163
	v_pk_add_f32 v[160:161], v[160:161], v[164:165] neg_lo:[0,1] neg_hi:[0,1]
	v_cvt_pk_bf16_f32 v158, v158, v159
	v_cvt_pk_bf16_f32 v159, v160, v161
	v_pk_mul_f32 v[160:161], v[172:173], v[176:177] op_sel_hi:[1,0]
	v_pk_mul_f32 v[164:165], v[168:169], v[176:177] op_sel_hi:[1,0]
	v_pk_fma_f32 v[160:161], v[146:147], v[160:161], v[12:13]
	v_mov_b32_e32 v169, v65
	v_med3_f32 v167, v160, s55, v228
	v_med3_f32 v168, v161, s55, v228
	v_cvt_pk_fp8_f32 v169, v167, v168
	v_pk_fma_f32 v[164:165], v[144:145], v[164:165], v[14:15]
	ds_write2st64_b64 v166, v[156:157], v[158:159] offset0:1 offset1:2
	v_med3_f32 v167, v164, s55, v228
	v_med3_f32 v168, v165, s55, v228
	v_cvt_pk_fp8_f32 v169, v167, v168 op_sel:[0,0,1]
	v_cvt_pk_bf16_f32 v156, v160, v161
	v_cvt_pk_bf16_f32 v157, v164, v165
	v_lshlrev_b32_e32 v158, 16, v156
	v_and_b32_e32 v159, 0xffff0000, v156
	v_pk_add_f32 v[158:159], v[160:161], v[158:159] neg_lo:[0,1] neg_hi:[0,1]
	v_lshlrev_b32_e32 v160, 16, v157
	v_and_b32_e32 v161, 0xffff0000, v157
	v_pk_add_f32 v[160:161], v[164:165], v[160:161] neg_lo:[0,1] neg_hi:[0,1]
	global_store_dword v[174:175], v181, off offset:3072
	global_store_dword v[174:175], v178, off offset:3328
	global_store_dword v[174:175], v169, off offset:3840
	v_cvt_pk_bf16_f32 v158, v158, v159
	v_cvt_pk_bf16_f32 v159, v160, v161
	ds_write2st64_b64 v64, v[162:163], v[156:157] offset0:14 offset1:15
	ds_write_b64 v166, v[158:159] offset:1536
	v_add_u32_e32 v64, 0, v232
	s_waitcnt lgkmcnt(0)
	s_barrier
	ds_read_b128 v[156:159], v64
	ds_read_b128 v[160:163], v64 offset:33024
	s_waitcnt lgkmcnt(1)
	v_mfma_f32_16x16x32_bf16 v[164:167], v[156:159], v[32:35], 0
	v_add_u32_e32 v168, s61, v232
	ds_read_b128 v[168:171], v168
	ds_read_b128 v[172:175], v64 offset:192
	v_mfma_f32_16x16x32_bf16 v[176:179], v[156:159], v[44:47], 0
	v_mfma_f32_16x16x32_bf16 v[180:183], v[156:159], v[40:43], 0
	v_mfma_f32_16x16x32_bf16 v[164:167], v[156:159], v[94:97], v[164:167]
	v_mfma_f32_16x16x32_bf16 v[176:179], v[156:159], v[36:39], v[176:179]
	v_mfma_f32_16x16x32_bf16 v[156:159], v[156:159], v[118:121], v[180:183]
	s_waitcnt lgkmcnt(1)
	v_mfma_f32_16x16x32_bf16 v[164:167], v[168:171], v[32:35], v[164:167]
	s_nop 2
	v_add_u32_e32 v180, s61, v233
	ds_read_b128 v[180:183], v180
	ds_read_b128 v[184:187], v239
	v_mfma_f32_16x16x32_bf16 v[176:179], v[168:171], v[44:47], v[176:179]
	v_mfma_f32_16x16x32_bf16 v[156:159], v[168:171], v[40:43], v[156:159]
	v_mfma_f32_16x16x32_bf16 v[168:171], v[160:163], v[32:35], 0
	v_mfma_f32_16x16x32_bf16 v[188:191], v[160:163], v[44:47], 0
	v_mfma_f32_16x16x32_bf16 v[192:195], v[160:163], v[40:43], 0
	v_mfma_f32_16x16x32_bf16 v[168:171], v[160:163], v[94:97], v[168:171]
	v_mfma_f32_16x16x32_bf16 v[188:191], v[160:163], v[36:39], v[188:191]
	v_mfma_f32_16x16x32_bf16 v[160:163], v[160:163], v[118:121], v[192:195]
	s_waitcnt lgkmcnt(1)
	v_mfma_f32_16x16x32_bf16 v[168:171], v[180:183], v[32:35], v[168:171]
	v_mfma_f32_16x16x32_bf16 v[188:191], v[180:183], v[44:47], v[188:191]
	v_mfma_f32_16x16x32_bf16 v[160:163], v[180:183], v[40:43], v[160:163]
	ds_read_b128 v[180:183], v64 offset:64
	ds_read_b128 v[192:195], v64 offset:128
	v_add_u32_e32 v64, 0, v233
	s_waitcnt lgkmcnt(1)
	v_mfma_f32_16x16x32_bf16 v[164:167], v[180:183], v[60:63], v[164:167]
	v_mfma_f32_16x16x32_bf16 v[176:179], v[180:183], v[48:51], v[176:179]
	v_mfma_f32_16x16x32_bf16 v[156:159], v[180:183], v[78:81], v[156:159]
	v_mfma_f32_16x16x32_bf16 v[164:167], v[180:183], v[52:55], v[164:167]
	v_mfma_f32_16x16x32_bf16 v[176:179], v[180:183], v[56:59], v[176:179]
	v_mfma_f32_16x16x32_bf16 v[156:159], v[180:183], v[70:73], v[156:159]
	v_mfma_f32_16x16x32_bf16 v[164:167], v[184:187], v[60:63], v[164:167]
	v_mfma_f32_16x16x32_bf16 v[176:179], v[184:187], v[48:51], v[176:179]
	v_mfma_f32_16x16x32_bf16 v[156:159], v[184:187], v[78:81], v[156:159]
	ds_read_b128 v[180:183], v64 offset:64
	ds_read_b128 v[184:187], v64 offset:128
	ds_read_b128 v[196:199], v240
	ds_read_b128 v[200:203], v64 offset:192
	v_add_u32_e32 v64, 0xc00, v238
	s_waitcnt lgkmcnt(3)
	v_mfma_f32_16x16x32_bf16 v[168:171], v[180:183], v[60:63], v[168:171]
	v_mfma_f32_16x16x32_bf16 v[188:191], v[180:183], v[48:51], v[188:191]
	v_mfma_f32_16x16x32_bf16 v[160:163], v[180:183], v[78:81], v[160:163]
	v_mfma_f32_16x16x32_bf16 v[168:171], v[180:183], v[52:55], v[168:171]
	v_mfma_f32_16x16x32_bf16 v[188:191], v[180:183], v[56:59], v[188:191]
	v_mfma_f32_16x16x32_bf16 v[160:163], v[180:183], v[70:73], v[160:163]
	v_mfma_f32_16x16x32_bf16 v[164:167], v[192:195], v[66:69], v[164:167]
	v_mfma_f32_16x16x32_bf16 v[176:179], v[192:195], v[102:105], v[176:179]
	v_mfma_f32_16x16x32_bf16 v[156:159], v[192:195], v[82:85], v[156:159]
	s_waitcnt lgkmcnt(1)
	v_mfma_f32_16x16x32_bf16 v[168:171], v[196:199], v[60:63], v[168:171]
	v_mfma_f32_16x16x32_bf16 v[188:191], v[196:199], v[48:51], v[188:191]
	v_mfma_f32_16x16x32_bf16 v[160:163], v[196:199], v[78:81], v[160:163]
	ds_read_b128 v[180:183], v241
	ds_read_b128 v[196:199], v242
	v_mfma_f32_16x16x32_bf16 v[164:167], v[192:195], v[74:77], v[164:167]
	v_mfma_f32_16x16x32_bf16 v[176:179], v[192:195], v[86:89], v[176:179]
	v_mfma_f32_16x16x32_bf16 v[156:159], v[192:195], v[90:93], v[156:159]
	s_waitcnt lgkmcnt(1)
	v_mfma_f32_16x16x32_bf16 v[164:167], v[180:183], v[66:69], v[164:167]
	v_mfma_f32_16x16x32_bf16 v[176:179], v[180:183], v[102:105], v[176:179]
	v_mfma_f32_16x16x32_bf16 v[156:159], v[180:183], v[82:85], v[156:159]
	v_mfma_f32_16x16x32_bf16 v[168:171], v[184:187], v[66:69], v[168:171]
	v_mfma_f32_16x16x32_bf16 v[180:183], v[184:187], v[102:105], v[188:191]
	v_mfma_f32_16x16x32_bf16 v[160:163], v[184:187], v[82:85], v[160:163]
	v_mfma_f32_16x16x32_bf16 v[168:171], v[184:187], v[74:77], v[168:171]
	v_mfma_f32_16x16x32_bf16 v[180:183], v[184:187], v[86:89], v[180:183]
	v_mfma_f32_16x16x32_bf16 v[160:163], v[184:187], v[90:93], v[160:163]
	ds_read_b128 v[184:187], v243
	ds_read_b128 v[188:191], v244
	s_waitcnt lgkmcnt(0)
	s_barrier
	v_mfma_f32_16x16x32_bf16 v[168:171], v[196:199], v[66:69], v[168:171]
	v_mfma_f32_16x16x32_bf16 v[180:183], v[196:199], v[102:105], v[180:183]
	v_mfma_f32_16x16x32_bf16 v[164:167], v[172:175], v[98:101], v[164:167]
	v_mfma_f32_16x16x32_bf16 v[176:179], v[172:175], v[106:109], v[176:179]
	v_mfma_f32_16x16x32_bf16 v[156:159], v[172:175], v[122:125], v[156:159]
	v_mfma_f32_16x16x32_bf16 v[160:163], v[196:199], v[82:85], v[160:163]
	v_mfma_f32_16x16x32_bf16 v[164:167], v[172:175], v[110:113], v[164:167]
	v_mfma_f32_16x16x32_bf16 v[176:179], v[172:175], v[114:117], v[176:179]
	v_mfma_f32_16x16x32_bf16 v[156:159], v[172:175], v[126:129], v[156:159]
	v_mfma_f32_16x16x32_bf16 v[168:171], v[200:203], v[98:101], v[168:171]
	v_mfma_f32_16x16x32_bf16 v[172:175], v[200:203], v[106:109], v[180:183]
	v_mfma_f32_16x16x32_bf16 v[160:163], v[200:203], v[122:125], v[160:163]
	v_mfma_f32_16x16x32_bf16 v[168:171], v[200:203], v[110:113], v[168:171]
	v_mfma_f32_16x16x32_bf16 v[172:175], v[200:203], v[114:117], v[172:175]
	v_mfma_f32_16x16x32_bf16 v[160:163], v[200:203], v[126:129], v[160:163]
	v_mfma_f32_16x16x32_bf16 v[164:167], v[184:187], v[98:101], v[164:167]
	v_mfma_f32_16x16x32_bf16 v[176:179], v[184:187], v[106:109], v[176:179]
	v_mfma_f32_16x16x32_bf16 v[168:171], v[188:191], v[98:101], v[168:171]
	v_mfma_f32_16x16x32_bf16 v[172:175], v[188:191], v[106:109], v[172:175]
	v_mfma_f32_16x16x32_bf16 v[156:159], v[184:187], v[122:125], v[156:159]
	s_nop 4
	ds_write2_b32 v238, v164, v176 offset1:16
	ds_write2_b32 v238, v166, v178 offset0:96 offset1:112
	s_nop 0
	ds_write2_b32 v238, v156, v165 offset0:32 offset1:48
	ds_write2_b32 v238, v177, v157 offset0:64 offset1:80
	ds_write2_b32 v238, v158, v167 offset0:128 offset1:144
	ds_write2_b32 v238, v179, v159 offset0:160 offset1:176
	v_mfma_f32_16x16x32_bf16 v[160:163], v[188:191], v[122:125], v[160:163]
	ds_write2_b32 v64, v168, v172 offset1:16
	ds_write2_b32 v64, v170, v174 offset0:96 offset1:112
	s_nop 5
	ds_write2_b32 v64, v160, v169 offset0:32 offset1:48
	ds_write2_b32 v64, v173, v161 offset0:64 offset1:80
	ds_write2_b32 v64, v162, v171 offset0:128 offset1:144
	ds_write2_b32 v64, v175, v163 offset0:160 offset1:176
	s_waitcnt lgkmcnt(0)
	s_barrier
	ds_read2st64_b32 v[156:157], v234 offset1:8
	ds_read2st64_b32 v[158:159], v234 offset0:16 offset1:24
	ds_read2st64_b32 v[160:161], v234 offset0:48 offset1:56
	ds_read2st64_b32 v[162:163], v234 offset0:64 offset1:72
	ds_read2st64_b32 v[164:165], v234 offset0:96 offset1:104
	ds_read2st64_b32 v[166:167], v234 offset0:112 offset1:120
	ds_read2st64_b32 v[168:169], v234 offset0:144 offset1:152
	s_waitcnt lgkmcnt(6)
	v_add_f32_e32 v64, 0, v156
	s_waitcnt lgkmcnt(5)
	v_add_f32_e32 v64, v64, v159
	s_waitcnt lgkmcnt(4)
	v_add_f32_e32 v64, v64, v160
	ds_read2st64_b32 v[170:171], v234 offset0:160 offset1:168
	s_waitcnt lgkmcnt(4)
	v_add_f32_e32 v64, v64, v163
	s_waitcnt lgkmcnt(3)
	v_add_f32_e32 v64, v64, v164
	s_waitcnt lgkmcnt(2)
	v_add_f32_e32 v64, v64, v167
	s_waitcnt lgkmcnt(1)
	v_add_f32_e32 v64, v64, v168
	ds_read2st64_b32 v[172:173], v234 offset0:32 offset1:40
	s_waitcnt lgkmcnt(1)
	v_add_f32_e32 v64, v64, v171
	ds_write_b32 v235, v64
	v_add_f32_e32 v64, 0, v157
	ds_read2st64_b32 v[156:157], v234 offset0:80 offset1:88
	ds_read2st64_b32 v[174:175], v234 offset0:128 offset1:136
	s_waitcnt lgkmcnt(3)
	v_add_f32_e32 v64, v64, v172
	v_add_f32_e32 v64, v64, v161
	ds_read2st64_b32 v[160:161], v234 offset0:176 offset1:184
	s_waitcnt lgkmcnt(2)
	v_add_f32_e32 v64, v64, v156
	v_add_f32_e32 v64, v64, v165
	s_waitcnt lgkmcnt(1)
	v_add_f32_e32 v64, v64, v174
	v_add_f32_e32 v64, v64, v169
	s_waitcnt lgkmcnt(0)
	v_add_f32_e32 v64, v64, v160
	v_add_u32_e32 v156, 0x800, v235
	ds_write_b32 v156, v64
	v_add_f32_e32 v64, 0, v158
	v_add_f32_e32 v64, v64, v173
	v_add_f32_e32 v64, v64, v162
	v_add_f32_e32 v64, v64, v157
	v_add_f32_e32 v64, v64, v166
	v_add_f32_e32 v64, v64, v175
	v_add_f32_e32 v64, v64, v170
	v_add_f32_e32 v64, v64, v161
	v_add_u32_e32 v156, 0x1000, v235
	ds_write_b32 v156, v64
	s_waitcnt lgkmcnt(0)
	s_barrier
	s_and_saveexec_b64 s[22:23], s[6:7]
	s_cbranch_execz .LBB0_696
	v_mov_b32_e32 v160, 0x24000
	ds_read_b128 v[160:163], v160
	ds_read_b128 v[156:159], v231
	v_mov_b32_e32 v176, 0x7f800000
	s_waitcnt lgkmcnt(0)
	v_pk_add_f32 v[156:157], v[156:157], v[160:161]
	s_nop 0
	v_cmp_gt_f32_e64 s[10:11], v157, v156
	v_add_f32_e32 v64, v158, v162
	v_add_f32_e32 v158, v159, v163
	v_cndmask_b32_e64 v159, v156, v157, s[10:11]
	v_cmp_gt_f32_e32 vcc, v64, v159
	s_nop 1
	v_cndmask_b32_e32 v159, v159, v64, vcc
	v_cmp_gt_f32_e64 s[8:9], v158, v159
	s_nop 1
	v_cndmask_b32_e64 v159, v159, v158, s[8:9]
	v_sub_f32_e32 v172, v156, v159
	v_sub_f32_e32 v156, v157, v159
	v_mul_f32_e32 v157, 0x3fb8aa3b, v156
	v_fma_f32 v160, v156, s33, -v157
	v_rndne_f32_e32 v161, v157
	v_fmac_f32_e32 v160, 0x32a5705f, v156
	v_sub_f32_e32 v157, v157, v161
	v_add_f32_e32 v157, v157, v160
	v_exp_f32_e32 v157, v157
	v_cvt_i32_f32_e32 v160, v161
	v_cmp_ngt_f32_e64 s[12:13], s54, v156
	v_sub_f32_e32 v64, v64, v159
	v_ldexp_f32 v157, v157, v160
	v_cndmask_b32_e64 v157, 0, v157, s[12:13]
	v_cmp_nlt_f32_e64 s[12:13], s85, v156
	v_mul_f32_e32 v156, 0x3fb8aa3b, v64
	v_rndne_f32_e32 v160, v156
	v_cndmask_b32_e64 v173, v176, v157, s[12:13]
	v_fma_f32 v157, v64, s33, -v156
	v_fmac_f32_e32 v157, 0x32a5705f, v64
	v_sub_f32_e32 v156, v156, v160
	v_add_f32_e32 v156, v156, v157
	v_exp_f32_e32 v156, v156
	v_cvt_i32_f32_e32 v157, v160
	v_cmp_ngt_f32_e64 s[12:13], s54, v64
	v_ldexp_f32 v156, v156, v157
	s_nop 0
	v_cndmask_b32_e64 v156, 0, v156, s[12:13]
	v_cmp_nlt_f32_e64 s[12:13], s85, v64
	s_nop 1
	v_cndmask_b32_e64 v64, v176, v156, s[12:13]
	v_sub_f32_e32 v156, v158, v159
	v_mul_f32_e32 v157, 0x3fb8aa3b, v156
	v_fma_f32 v158, v156, s33, -v157
	v_rndne_f32_e32 v159, v157
	v_fmac_f32_e32 v158, 0x32a5705f, v156
	v_sub_f32_e32 v157, v157, v159
	v_add_f32_e32 v157, v157, v158
	v_exp_f32_e32 v157, v157
	v_cvt_i32_f32_e32 v158, v159
	v_cmp_ngt_f32_e64 s[12:13], s54, v156
	v_ldexp_f32 v157, v157, v158
	s_nop 0
	v_cndmask_b32_e64 v157, 0, v157, s[12:13]
	v_cmp_nlt_f32_e64 s[12:13], s85, v156
	v_cndmask_b32_e64 v156, 0, 8, s[10:11]
	v_cndmask_b32_e64 v156, v156, 16, vcc
	v_cndmask_b32_e64 v175, v156, 24, s[8:9]
	v_lshlrev_b32_e32 v168, 2, v175
	v_add_u32_e32 v160, v231, v168
	v_cndmask_b32_e64 v174, v176, v157, s[12:13]
	ds_read_b128 v[156:159], v160 offset:16
	ds_read_b128 v[160:163], v160 offset:32
	v_add_u32_e32 v164, 0x24000, v168
	ds_read_b128 v[168:171], v164 offset:16
	ds_read_b128 v[164:167], v164 offset:32
	v_cmp_ngt_f32_e32 vcc, s54, v172
	s_mov_b32 s12, 0xff61b1e6
	s_waitcnt lgkmcnt(0)
	v_add_f32_e32 v160, v160, v164
	v_mul_f32_e32 v164, 0x3fb8aa3b, v172
	v_add_f32_e32 v161, v161, v165
	v_add_f32_e32 v162, v162, v166
	v_fma_f32 v165, v172, s33, -v164
	v_rndne_f32_e32 v166, v164
	v_fmac_f32_e32 v165, 0x32a5705f, v172
	v_sub_f32_e32 v164, v164, v166
	v_add_f32_e32 v164, v164, v165
	v_exp_f32_e32 v164, v164
	v_cvt_i32_f32_e32 v165, v166
	v_pk_add_f32 v[156:157], v[156:157], v[168:169]
	v_add_f32_e32 v158, v158, v170
	v_add_f32_e32 v159, v159, v171
	v_ldexp_f32 v164, v164, v165
	v_cndmask_b32_e32 v164, 0, v164, vcc
	v_cmp_nlt_f32_e32 vcc, s85, v172
	v_add_f32_e32 v163, v163, v167
	v_cmp_nlt_f32_e64 s[12:13], s12, v156
	v_cndmask_b32_e32 v164, v176, v164, vcc
	v_cmp_gt_f32_e32 vcc, v157, v156
	v_add_f32_e32 v164, v164, v173
	v_add_f32_e32 v64, v64, v164
	v_cndmask_b32_e32 v165, v156, v157, vcc
	v_cndmask_b32_e64 v164, 0, 1, vcc
	v_cmp_gt_f32_e32 vcc, v158, v165
	v_mov_b32_e32 v166, 0xff61b1e6
	v_add_f32_e32 v64, v174, v64
	v_cndmask_b32_e32 v165, v165, v158, vcc
	v_cndmask_b32_e64 v164, v164, 2, vcc
	v_cmp_gt_f32_e32 vcc, v159, v165
	s_nop 1
	v_cndmask_b32_e32 v165, v165, v159, vcc
	v_cndmask_b32_e64 v164, v164, 3, vcc
	v_cmp_gt_f32_e32 vcc, v160, v165
	s_nop 1
	v_cndmask_b32_e32 v165, v165, v160, vcc
	v_cndmask_b32_e64 v164, v164, 4, vcc
	v_cmp_gt_f32_e32 vcc, v161, v165
	s_nop 1
	v_cndmask_b32_e32 v165, v165, v161, vcc
	v_cndmask_b32_e64 v164, v164, 5, vcc
	v_cmp_gt_f32_e32 vcc, v162, v165
	s_nop 1
	v_cndmask_b32_e32 v165, v165, v162, vcc
	v_cndmask_b32_e64 v164, v164, 6, vcc
	v_cmp_ngt_f32_e64 s[8:9], v163, v165
	s_nop 1
	v_cndmask_b32_e64 v164, 7, v164, s[8:9]
	v_cmp_eq_u32_e64 s[10:11], 0, v164
	s_or_b64 s[12:13], s[10:11], s[12:13]
	v_cndmask_b32_e64 v156, v156, v166, s[12:13]
	v_cmp_ne_u32_e64 s[12:13], 1, v164
	v_cmp_gt_f32_e64 s[14:15], v157, v156
	s_and_b64 s[12:13], s[12:13], s[14:15]
	s_or_b64 s[10:11], s[10:11], s[12:13]
	v_cndmask_b32_e64 v156, v156, v157, s[12:13]
	v_cndmask_b32_e64 v157, 0, 1, s[10:11]
	v_cmp_ne_u32_e64 s[10:11], 2, v164
	v_cmp_gt_f32_e64 s[12:13], v158, v156
	s_and_b64 s[10:11], s[10:11], s[12:13]
	v_cndmask_b32_e64 v156, v156, v158, s[10:11]
	v_cndmask_b32_e64 v157, v157, 2, s[10:11]
	v_cmp_ne_u32_e64 s[10:11], 3, v164
	v_cmp_gt_f32_e64 s[12:13], v159, v156
	s_and_b64 s[10:11], s[10:11], s[12:13]
	v_cndmask_b32_e64 v156, v156, v159, s[10:11]
	v_cndmask_b32_e64 v157, v157, 3, s[10:11]
	v_cmp_ne_u32_e64 s[10:11], 4, v164
	v_cmp_gt_f32_e64 s[12:13], v160, v156
	s_and_b64 s[10:11], s[10:11], s[12:13]
	v_cndmask_b32_e64 v156, v156, v160, s[10:11]
	v_cndmask_b32_e64 v157, v157, 4, s[10:11]
	v_cmp_ne_u32_e64 s[10:11], 5, v164
	v_cmp_gt_f32_e64 s[12:13], v161, v156
	s_and_b64 s[10:11], s[10:11], s[12:13]
	v_cndmask_b32_e64 v156, v156, v161, s[10:11]
	v_cndmask_b32_e64 v157, v157, 5, s[10:11]
	s_and_b64 s[10:11], vcc, s[8:9]
	v_cmp_ngt_f32_e32 vcc, v162, v156
	s_or_b64 vcc, s[10:11], vcc
	v_cndmask_b32_e64 v165, v163, v165, s[8:9]
	v_cndmask_b32_e32 v156, v162, v156, vcc
	v_cndmask_b32_e32 v157, 6, v157, vcc
	v_cmp_gt_f32_e32 vcc, v163, v156
	s_and_b64 vcc, s[8:9], vcc
	s_nop 0
	v_cndmask_b32_e64 v159, v157, 7, vcc
	v_div_scale_f32 v157, s[8:9], v64, v64, 1.0
	v_rcp_f32_e32 v158, v157
	v_cndmask_b32_e32 v156, v156, v163, vcc
	v_sub_f32_e32 v156, v156, v165
	v_add_u32_e32 v159, v159, v175
	v_fma_f32 v160, -v157, v158, 1.0
	v_fmac_f32_e32 v158, v160, v158
	v_div_scale_f32 v160, vcc, 1.0, v64, 1.0
	v_mul_f32_e32 v161, v160, v158
	v_fma_f32 v162, -v157, v161, v160
	v_fmac_f32_e32 v161, v162, v158
	v_fma_f32 v157, -v157, v161, v160
	v_div_fmas_f32 v157, v157, v158, v161
	v_div_fixup_f32 v64, v157, v64, 1.0
	v_mul_f32_e32 v157, 0x3fb8aa3b, v156
	v_fma_f32 v158, v156, s33, -v157
	v_rndne_f32_e32 v160, v157
	v_fmac_f32_e32 v158, 0x32a5705f, v156
	v_sub_f32_e32 v157, v157, v160
	v_add_f32_e32 v157, v157, v158
	v_exp_f32_e32 v157, v157
	v_cvt_i32_f32_e32 v158, v160
	v_cmp_ngt_f32_e32 vcc, s54, v156
	v_ldexp_f32 v157, v157, v158
	s_nop 0
	v_cndmask_b32_e32 v157, 0, v157, vcc
	v_cmp_nlt_f32_e32 vcc, s85, v156
	s_nop 1
	v_cndmask_b32_e32 v157, v176, v157, vcc
	v_add_f32_e32 v156, 1.0, v157
	v_div_scale_f32 v158, s[8:9], v156, v156, 1.0
	v_rcp_f32_e32 v160, v158
	s_add_i32 s8, 0, 0x22c00
	v_fma_f32 v161, -v158, v160, 1.0
	v_fmac_f32_e32 v160, v161, v160
	v_div_scale_f32 v161, vcc, 1.0, v156, 1.0
	v_mul_f32_e32 v162, v161, v160
	v_fma_f32 v163, -v158, v162, v161
	v_fmac_f32_e32 v162, v163, v160
	v_fma_f32 v158, -v158, v162, v161
	v_div_fmas_f32 v158, v158, v160, v162
	v_div_fixup_f32 v156, v158, v156, 1.0
	v_or_b32_e32 v158, v164, v175
	ds_write_b64 v237, v[158:159]
	v_lshl_add_u32 v158, v158, 2, s8
	v_mov_b32_e32 v160, 1
	ds_add_rtn_u32 v158, v158, v160
	v_mul_f32_e32 v157, v157, v156
	v_pk_mul_f32 v[156:157], v[64:65], v[156:157] op_sel_hi:[0,1]
	s_waitcnt lgkmcnt(0)
	ds_write_b32 v237, v158 offset:2048
	v_lshl_add_u32 v158, v159, 2, s8
	ds_add_rtn_u32 v158, v158, v160
	s_waitcnt lgkmcnt(0)
	ds_write_b32 v237, v158 offset:2052
	v_lshl_add_u64 v[158:159], s[42:43], 0, v[148:149]
	global_store_dwordx2 v[158:159], v[156:157], off
	s_branch .LBB0_696

.LBB0_903:
	v_mov_b32_e32 v129, 0
	s_andn2_b64 vcc, exec, s[12:13]
	v_mov_b32_e32 v128, v129
	v_mov_b32_e32 v127, v129
	v_mov_b32_e32 v126, v129
	v_mov_b32_e32 v125, v129
	v_mov_b32_e32 v124, v129
	v_mov_b32_e32 v123, v129
	v_mov_b32_e32 v122, v129
	v_mov_b32_e32 v113, v129
	v_mov_b32_e32 v112, v129
	v_mov_b32_e32 v111, v129
	v_mov_b32_e32 v110, v129
	v_mov_b32_e32 v109, v129
	v_mov_b32_e32 v108, v129
	v_mov_b32_e32 v107, v129
	v_mov_b32_e32 v106, v129
	v_mov_b32_e32 v97, v129
	v_mov_b32_e32 v96, v129
	v_mov_b32_e32 v95, v129
	v_mov_b32_e32 v94, v129
	v_mov_b32_e32 v93, v129
	v_mov_b32_e32 v92, v129
	v_mov_b32_e32 v91, v129
	v_mov_b32_e32 v90, v129
	v_mov_b32_e32 v81, v129
	v_mov_b32_e32 v80, v129
	v_mov_b32_e32 v79, v129
	v_mov_b32_e32 v78, v129
	v_mov_b32_e32 v77, v129
	v_mov_b32_e32 v76, v129
	v_mov_b32_e32 v75, v129
	v_mov_b32_e32 v74, v129
	v_mov_b32_e32 v121, v129
	v_mov_b32_e32 v120, v129
	v_mov_b32_e32 v119, v129
	v_mov_b32_e32 v118, v129
	v_mov_b32_e32 v117, v129
	v_mov_b32_e32 v116, v129
	v_mov_b32_e32 v115, v129
	v_mov_b32_e32 v114, v129
	v_mov_b32_e32 v105, v129
	v_mov_b32_e32 v104, v129
	v_mov_b32_e32 v103, v129
	v_mov_b32_e32 v102, v129
	v_mov_b32_e32 v101, v129
	v_mov_b32_e32 v100, v129
	v_mov_b32_e32 v99, v129
	v_mov_b32_e32 v98, v129
	v_mov_b32_e32 v89, v129
	v_mov_b32_e32 v88, v129
	v_mov_b32_e32 v87, v129
	v_mov_b32_e32 v86, v129
	v_mov_b32_e32 v85, v129
	v_mov_b32_e32 v84, v129
	v_mov_b32_e32 v83, v129
	v_mov_b32_e32 v82, v129
	v_mov_b32_e32 v73, v129
	v_mov_b32_e32 v72, v129
	v_mov_b32_e32 v71, v129
	v_mov_b32_e32 v70, v129
	v_mov_b32_e32 v69, v129
	v_mov_b32_e32 v68, v129
	v_mov_b32_e32 v67, v129
	v_mov_b32_e32 v66, v129
	v_mov_b32_e32 v63, v129
	v_mov_b32_e32 v62, v129
	v_mov_b32_e32 v61, v129
	v_mov_b32_e32 v60, v129
	v_mov_b32_e32 v59, v129
	v_mov_b32_e32 v58, v129
	v_mov_b32_e32 v57, v129
	v_mov_b32_e32 v56, v129
	v_mov_b32_e32 v47, v129
	v_mov_b32_e32 v46, v129
	v_mov_b32_e32 v45, v129
	v_mov_b32_e32 v44, v129
	v_mov_b32_e32 v43, v129
	v_mov_b32_e32 v42, v129
	v_mov_b32_e32 v41, v129
	v_mov_b32_e32 v40, v129
	v_mov_b32_e32 v31, v129
	v_mov_b32_e32 v30, v129
	v_mov_b32_e32 v29, v129
	v_mov_b32_e32 v28, v129
	v_mov_b32_e32 v27, v129
	v_mov_b32_e32 v26, v129
	v_mov_b32_e32 v25, v129
	v_mov_b32_e32 v24, v129
	v_mov_b32_e32 v15, v129
	v_mov_b32_e32 v14, v129
	v_mov_b32_e32 v13, v129
	v_mov_b32_e32 v12, v129
	v_mov_b32_e32 v11, v129
	v_mov_b32_e32 v10, v129
	v_mov_b32_e32 v9, v129
	v_mov_b32_e32 v8, v129
	v_mov_b32_e32 v55, v129
	v_mov_b32_e32 v54, v129
	v_mov_b32_e32 v53, v129
	v_mov_b32_e32 v52, v129
	v_mov_b32_e32 v51, v129
	v_mov_b32_e32 v50, v129
	v_mov_b32_e32 v49, v129
	v_mov_b32_e32 v48, v129
	v_mov_b32_e32 v39, v129
	v_mov_b32_e32 v38, v129
	v_mov_b32_e32 v37, v129
	v_mov_b32_e32 v36, v129
	v_mov_b32_e32 v35, v129
	v_mov_b32_e32 v34, v129
	v_mov_b32_e32 v33, v129
	v_mov_b32_e32 v32, v129
	v_mov_b32_e32 v23, v129
	v_mov_b32_e32 v22, v129
	v_mov_b32_e32 v21, v129
	v_mov_b32_e32 v20, v129
	v_mov_b32_e32 v19, v129
	v_mov_b32_e32 v18, v129
	v_mov_b32_e32 v17, v129
	v_mov_b32_e32 v16, v129
	v_mov_b32_e32 v7, v129
	v_mov_b32_e32 v6, v129
	v_mov_b32_e32 v5, v129
	v_mov_b32_e32 v4, v129
	v_mov_b32_e32 v3, v129
	v_mov_b32_e32 v2, v129
	v_mov_b32_e32 v1, v129
	v_mov_b32_e32 v0, v129
	s_cbranch_vccnz .LBB0_907
	s_add_u32 s49, s22, 0x100
	v_mov_b32_e32 v0, 0
	s_mov_b32 s45, s63
	s_addc_u32 s87, s23, 0
	s_mov_b32 s24, 0
	v_mov_b32_e32 v1, v0
	v_mov_b32_e32 v2, v0
	v_mov_b32_e32 v3, v0
	v_mov_b32_e32 v4, v0
	v_mov_b32_e32 v5, v0
	v_mov_b32_e32 v6, v0
	v_mov_b32_e32 v7, v0
	v_mov_b32_e32 v8, v0
	v_mov_b32_e32 v9, v0
	v_mov_b32_e32 v10, v0
	v_mov_b32_e32 v11, v0
	v_mov_b32_e32 v12, v0
	v_mov_b32_e32 v13, v0
	v_mov_b32_e32 v14, v0
	v_mov_b32_e32 v15, v0
	v_mfma_f32_32x32x16_bf16 v[16:31], v[0:3], v[0:3], 0
	v_mfma_f32_32x32x16_bf16 v[32:47], v[0:3], v[0:3], 0
	v_mfma_f32_32x32x16_bf16 v[48:63], v[0:3], v[0:3], 0
	v_mfma_f32_32x32x16_bf16 v[66:81], v[0:3], v[0:3], 0
	v_mfma_f32_32x32x16_bf16 v[82:97], v[0:3], v[0:3], 0
	v_mfma_f32_32x32x16_bf16 v[98:113], v[0:3], v[0:3], 0
	v_mfma_f32_32x32x16_bf16 v[114:129], v[0:3], v[0:3], 0
